# bundle6 + N2 (layer>0): next iteration rows 0,1 loads issued before the router stage (saddr-form loads, copies at loop top)
# speedup vs baseline: 1.0130x; 1.0015x over previous
.LBB0_693:
	v_readlane_b32 s22, v254, 12
	s_mov_b32 s6, s22
	s_waitcnt vmcnt(0)
	s_barrier
	v_mbcnt_lo_u32_b32 v0, -1, 0
	v_mbcnt_hi_u32_b32 v0, -1, v0
	v_mbcnt_lo_u32_b32 v222, -1, 0
	v_mbcnt_hi_u32_b32 v222, -1, v222
	s_nop 0
	v_lshl_add_u32 v130, s22, 6, v222
	v_cmp_gt_i32_e64 s[6:7], 32, v130
	v_lshl_add_u32 v230, v130, 2, 0
	s_barrier
	s_and_saveexec_b64 s[8:9], s[6:7]
	v_add_u32_e32 v0, 0x22c00, v230
	ds_write_b32 v0, v65
	s_or_b64 exec, exec, s[8:9]
	v_readlane_b32 s18, v255, 37
	v_readlane_b32 s19, v255, 38
	s_mov_b32 s19, s67
	s_lshl_b64 s[10:11], s[18:19], 3
	s_mul_i32 s9, s18, 0x30000
	v_readlane_b32 s12, v255, 26
	s_mul_hi_u32 s8, s18, 0x30000
	v_readlane_b32 s13, v255, 27
	s_add_u32 s16, s12, s9
	s_addc_u32 s17, s13, s8
	s_mov_b32 s8, s18
	s_add_u32 s14, s16, 0x18000
	v_writelane_b32 v255, s8, 37
	v_readlane_b32 s28, v254, 13
	s_addc_u32 s15, s17, 0
	v_writelane_b32 v255, s9, 38
	s_add_i32 s8, s22, s28
	s_ashr_i32 s9, s8, 8
	s_lshl_b32 s66, s18, 2
	s_ashr_i32 s12, s9, 31
	s_add_u32 s9, s10, s9
	s_addc_u32 s10, s11, s12
	s_mulk_i32 s10, 0x6000
	s_mul_hi_u32 s11, s9, 0x6000
	s_add_i32 s11, s11, s10
	s_mulk_i32 s9, 0x6000
	v_readlane_b32 s12, v255, 28
	v_readlane_b32 s13, v255, 29
	s_add_u32 s9, s12, s9
	s_addc_u32 s23, s13, s11
	v_readlane_b32 s26, v254, 16
	v_readlane_b32 s20, v255, 39
	v_readlane_b32 s27, v254, 17
	s_load_dwordx2 s[18:19], s[26:27], 48
	s_waitcnt lgkmcnt(0)
	v_readlane_b32 s21, v255, 40
	s_add_u32 s20, s18, s20
	s_addc_u32 s21, s19, s21
	v_and_b32_e32 v153, 63, v222
	s_load_dwordx2 s[12:13], s[26:27], 0x98
	s_waitcnt lgkmcnt(0)
	s_add_u32 s18, s9, 0x4000
	s_load_dwordx2 s[10:11], s[26:27], 0xa8
	s_waitcnt lgkmcnt(0)
	s_addc_u32 s19, s23, 0
	v_lshlrev_b32_e32 v152, 4, v153
	global_load_dwordx4 v[60:63], v152, s[18:19]
	v_or_b32_e32 v8, 0x400, v152
	global_load_dwordx4 v[66:69], v8, s[18:19]
	global_load_dwordx4 v[70:73], v152, s[20:21]
	global_load_dwordx4 v[74:77], v152, s[20:21] offset:1024
	global_load_dwordx4 v[142:145], v152, s[20:21] offset:2048
	global_load_dwordx4 v[146:149], v152, s[20:21] offset:3072
	s_add_u32 s20, s9, 0x3000
	s_addc_u32 s21, s23, 0
	s_add_u32 s24, s9, 0x2000
	s_addc_u32 s25, s23, 0
	v_or_b32_e32 v24, 0x800, v152
	v_or_b32_e32 v42, 0xc00, v152
	global_load_dwordx4 v[0:3], v8, s[24:25]
	global_load_dwordx4 v[154:157], v24, s[18:19]
	global_load_dwordx4 v[4:7], v152, s[20:21]
	s_nop 0
	global_load_dwordx4 v[8:11], v8, s[20:21]
	s_nop 0
	global_load_dwordx4 v[158:161], v42, s[18:19]
	global_load_dwordx4 v[12:15], v42, s[20:21]
	v_and_b32_e32 v162, 15, v222
	s_lshl_b32 s9, s22, 7
	v_bfe_u32 v163, v222, 4, 2
	v_lshlrev_b32_e32 v64, 10, v162
	s_ashr_i32 s18, s9, 31
	v_mov_b32_e32 v103, v65
	v_or_b32_e32 v102, 0x4000, v64
	v_lshl_or_b32 v120, v163, 3, s9
	v_mov_b32_e32 v121, s18
	v_mov_b32_e32 v119, v65
	v_or_b32_e32 v118, 0x8000, v64
	v_or_b32_e32 v28, 32, v120
	v_lshl_add_u64 v[32:33], v[120:121], 0, v[102:103]
	v_mov_b32_e32 v29, s18
	v_lshl_add_u64 v[30:31], v[120:121], 0, v[64:65]
	v_lshl_add_u64 v[34:35], v[120:121], 0, v[118:119]
	v_lshlrev_b64 v[32:33], 1, v[32:33]
	v_lshl_add_u64 v[36:37], v[28:29], 0, v[64:65]
	v_lshl_add_u64 v[38:39], v[28:29], 0, v[102:103]
	v_lshlrev_b64 v[30:31], 1, v[30:31]
	v_lshlrev_b64 v[34:35], 1, v[34:35]
	v_lshl_add_u64 v[28:29], v[28:29], 0, v[118:119]
	v_lshl_add_u64 v[40:41], s[14:15], 0, v[32:33]
	v_lshl_add_u64 v[52:53], v[36:37], 1, s[14:15]
	v_lshl_add_u64 v[56:57], v[38:39], 1, s[14:15]
	global_load_dwordx4 v[16:19], v152, s[24:25]
	global_load_dwordx4 v[20:23], v24, s[20:21]
	s_nop 0
	global_load_dwordx4 v[24:27], v24, s[24:25]
	v_lshl_add_u64 v[98:99], s[16:17], 0, v[30:31]
	v_lshl_add_u64 v[94:95], s[14:15], 0, v[30:31]
	v_lshl_add_u64 v[106:107], s[16:17], 0, v[32:33]
	v_lshl_add_u64 v[122:123], s[16:17], 0, v[34:35]
	v_lshl_add_u64 v[124:125], s[14:15], 0, v[34:35]
	v_lshl_add_u64 v[80:81], v[28:29], 1, s[14:15]
	global_load_dwordx4 v[28:31], v42, s[24:25]
	global_load_dwordx4 v[32:35], v[98:99], off
	global_load_dwordx4 v[36:39], v[40:41], off
	s_nop 0
	global_load_dwordx4 v[40:43], v[122:123], off
	global_load_dwordx4 v[44:47], v[106:107], off
	global_load_dwordx4 v[48:51], v[106:107], off offset:64
	s_nop 0
	global_load_dwordx4 v[52:55], v[52:53], off
	s_nop 0
	global_load_dwordx4 v[56:59], v[56:57], off
	v_or_b32_e32 v78, 64, v120
	v_mov_b32_e32 v79, s18
	v_or_b32_e32 v120, 0x60, v120
	v_lshl_add_u64 v[88:89], v[78:79], 0, v[118:119]
	v_lshl_add_u64 v[104:105], v[120:121], 0, v[64:65]
	v_lshl_add_u64 v[112:113], v[120:121], 0, v[102:103]
	v_lshl_add_u64 v[126:127], v[120:121], 0, v[118:119]
	v_lshl_add_u64 v[90:91], v[88:89], 1, s[14:15]
	v_lshl_add_u64 v[110:111], v[104:105], 1, s[14:15]
	v_lshl_add_u64 v[114:115], v[112:113], 1, s[14:15]
	v_lshl_add_u64 v[126:127], v[126:127], 1, s[14:15]
	s_lshl_b32 s16, s22, 8
	s_ashr_i32 s9, s8, 31
	v_readlane_b32 s21, v255, 7
	s_movk_i32 s20, 0xc0
	v_lshlrev_b32_e32 v131, 3, v153
	v_add_u32_e32 v236, s61, v131
	s_waitcnt vmcnt(22)
	v_pk_add_f32 v[60:61], v[60:61], 1.0 op_sel_hi:[1,0]
	s_waitcnt vmcnt(21)
	v_pk_add_f32 v[66:67], v[66:67], 1.0 op_sel_hi:[1,0]
	s_waitcnt vmcnt(20)
	v_pk_mul_f32 v[134:135], v[70:71], v[60:61]
	v_lshl_add_u64 v[70:71], v[78:79], 0, v[64:65]
	v_pk_add_f32 v[62:63], v[62:63], 1.0 op_sel_hi:[1,0]
	v_pk_add_f32 v[68:69], v[68:69], 1.0 op_sel_hi:[1,0]
	s_waitcnt vmcnt(19)
	v_pk_mul_f32 v[138:139], v[74:75], v[66:67]
	v_lshl_add_u64 v[74:75], v[70:71], 1, s[14:15]
	v_pk_mul_f32 v[132:133], v[72:73], v[62:63]
	v_pk_mul_f32 v[136:137], v[76:77], v[68:69]
	global_load_dwordx4 v[60:63], v[98:99], off offset:64
	global_load_dwordx4 v[66:69], v[98:99], off offset:128
	global_load_dwordx4 v[70:73], v[80:81], off
	s_nop 0
	global_load_dwordx4 v[74:77], v[74:75], off
	v_lshl_add_u64 v[80:81], v[78:79], 0, v[102:103]
	v_lshl_add_u64 v[86:87], v[80:81], 1, s[14:15]
	global_load_dwordx4 v[78:81], v[122:123], off offset:64
	global_load_dwordx4 v[82:85], v[122:123], off offset:128
	s_nop 0
	global_load_dwordx4 v[86:89], v[86:87], off
	s_nop 0
	global_load_dwordx4 v[90:93], v[90:91], off
	s_nop 0
	global_load_dwordx4 v[94:97], v[94:95], off
	s_nop 0
	global_load_dwordx4 v[98:101], v[98:99], off offset:192
	s_nop 0
	global_load_dwordx4 v[102:105], v[106:107], off offset:128
	s_nop 0
	global_load_dwordx4 v[106:109], v[106:107], off offset:192
	s_nop 0
	global_load_dwordx4 v[110:113], v[110:111], off
	s_nop 0
	global_load_dwordx4 v[114:117], v[114:115], off
	s_nop 0
	global_load_dwordx4 v[118:121], v[124:125], off
	s_nop 0
	global_load_dwordx4 v[122:125], v[122:123], off offset:192
	s_waitcnt vmcnt(31)
	v_pk_add_f32 v[140:141], v[156:157], 1.0 op_sel_hi:[1,0]
	global_load_dwordx4 v[126:129], v[126:127], off
	v_pk_mul_f32 v[140:141], v[144:145], v[140:141]
	s_waitcnt vmcnt(29)
	v_pk_add_f32 v[144:145], v[160:161], 1.0 op_sel_hi:[1,0]
	v_pk_add_f32 v[150:151], v[154:155], 1.0 op_sel_hi:[1,0]
	v_pk_mul_f32 v[144:145], v[148:149], v[144:145]
	v_and_or_b32 v148, v222, 48, s16
	s_lshl_b32 s16, s22, 5
	v_lshl_or_b32 v149, v163, 2, s16
	s_lshl_b64 s[16:17], s[66:67], 2
	s_add_u32 s16, s12, s16
	s_addc_u32 s17, s13, s17
	v_readlane_b32 s12, v255, 41
	v_pk_mul_f32 v[142:143], v[142:143], v[150:151]
	v_pk_add_f32 v[150:151], v[158:159], 1.0 op_sel_hi:[1,0]
	v_readlane_b32 s13, v255, 42
	s_add_u32 s18, s10, s12
	v_pk_mul_f32 v[146:147], v[146:147], v[150:151]
	s_addc_u32 s19, s11, s13
	s_movk_i32 s11, 0x810
	v_mov_b32_e32 v151, 0x8100
	v_mad_u32_u24 v151, v162, s11, v151
	v_or_b32_e32 v154, 64, v148
	v_mad_u32_u24 v232, v162, s11, v148
	v_add_u32_e32 v233, v151, v148
	v_mad_u32_u24 v157, v162, s11, v154
	v_add_u32_e32 v158, v154, v151
	v_or_b32_e32 v154, 0x80, v148
	v_or_b32_e32 v148, 0xc0, v148
	v_lshl_add_u32 v156, v162, 2, 0
	v_mad_u32_u24 v159, v162, s11, v154
	v_mad_u32_u24 v161, v162, s11, v148
	v_add_u32_e32 v162, v148, v151
	v_lshlrev_b32_e32 v148, 2, v130
	v_add_u32_e32 v234, 0, v148
	v_add_u32_e32 v235, s21, v148
	v_lshlrev_b32_e32 v148, 3, v222
	v_mul_lo_u32 v64, v130, s20
	v_ashrrev_i32_e32 v150, 2, v130
	s_mul_i32 s10, s22, 0x2040
	v_add_u32_e32 v160, v154, v151
	v_and_b32_e32 v151, 24, v148
	s_load_dwordx2 s[14:15], s[26:27], 0
	s_waitcnt lgkmcnt(0)
	v_add_u32_e32 v231, s21, v64
	v_add_u32_e32 v64, s28, v150
	s_add_i32 s24, s10, 0x810
	s_add_i32 s25, s10, 0x1020
	s_add_i32 s26, s10, 0x1830
	s_add_i32 s27, s10, 0
	s_add_i32 s28, s61, s10
	v_lshl_or_b32 v148, v150, 8, v151
	v_readlane_b32 s10, v255, 8
	v_mul_lo_u32 v163, v149, s20
	s_add_i32 s29, s61, s24
	v_add_u32_e32 v237, s10, v148
	v_lshlrev_b64 v[148:149], 8, v[64:65]
	v_or_b32_e32 v148, v148, v151
	s_mov_b64 s[10:11], 0x300000
	v_lshl_add_u64 v[148:149], v[148:149], 0, s[10:11]
	s_lshl_b64 s[10:11], s[8:9], 15
	s_add_i32 s30, s61, s25
	s_add_i32 s31, s61, s26
	v_lshl_or_b32 v150, v153, 2, s10
	v_mov_b32_e32 v151, s11
	s_lshl_b64 s[10:11], s[8:9], 17
	s_add_u32 s10, s14, s10
	v_mov_b32_e32 v153, v65
	s_addc_u32 s11, s15, s11
	s_lshl_b64 s[8:9], s[8:9], 16
	v_lshl_add_u64 v[152:153], s[10:11], 0, v[152:153]
	v_or_b32_e32 v154, s8, v131
	v_mov_b32_e32 v155, s9
	s_mov_b64 s[20:21], 0
	v_add_u32_e32 v238, v156, v163
	v_add_u32_e32 v239, s61, v157
	v_add_u32_e32 v240, s61, v158
	v_add_u32_e32 v241, s61, v159
	v_add_u32_e32 v242, s61, v160
	v_add_u32_e32 v243, s61, v161
	v_add_u32_e32 v244, s61, v162
	v_mbcnt_lo_u32_b32 v200, -1, 0
	v_mbcnt_hi_u32_b32 v200, -1, v200
	v_lshlrev_b32_e32 v201, 2, v200
	v_cmp_gt_u32_e32 vcc, 4, v200
	s_and_saveexec_b64 s[8:9], vcc
	global_load_dword v202, v201, s[16:17]
	s_or_b64 exec, exec, s[8:9]
	v_cmp_gt_u32_e32 vcc, 32, v200
	s_and_saveexec_b64 s[8:9], vcc
	global_load_dword v203, v201, s[18:19]
	s_or_b64 exec, exec, s[8:9]
	s_waitcnt vmcnt(0)
	v_add_u32_e32 v204, 0x24000, v201
	v_cmp_gt_u32_e32 vcc, 4, v200
	s_and_saveexec_b64 s[8:9], vcc
	ds_write_b32 v204, v202
	s_or_b64 exec, exec, s[8:9]
	v_cmp_gt_u32_e32 vcc, 32, v200
	s_and_saveexec_b64 s[8:9], vcc
	ds_write_b32 v204, v203 offset:16
	s_or_b64 exec, exec, s[8:9]
	s_waitcnt lgkmcnt(0)
	s_add_u32 s98, s42, 0x40100000
	s_addc_u32 s99, s43, 0
	s_add_u32 s100, s42, 0x6800000
	s_addc_u32 s101, s43, 0
	s_branch .LBB0_697

.LBB0_697:
	s_and_b64 vcc, exec, s[86:87]
	v_lshl_add_u64 v[164:165], s[42:43], 0, v[154:155]
	s_cbranch_vccz .LBB0_747
	s_cmp_eq_u32 s20, 0
	s_cbranch_scc1 .Ln2pf_full
	v_add_u32_e32 v245, 0x1000, v154
	global_load_dwordx2 v[202:203], v154, s[98:99] offset:3584 nt
	global_load_dwordx2 v[206:207], v154, s[100:101] offset:3584
	global_load_dwordx2 v[176:177], v245, s[98:99] nt
	global_load_dwordx2 v[180:181], v245, s[100:101]
	global_load_dwordx2 v[178:179], v245, s[98:99] offset:512 nt
	global_load_dwordx2 v[184:185], v245, s[100:101] offset:512
	global_load_dwordx2 v[182:183], v245, s[98:99] offset:1024 nt
	global_load_dwordx2 v[188:189], v245, s[100:101] offset:1024
	global_load_dwordx2 v[186:187], v245, s[98:99] offset:1536 nt
	global_load_dwordx2 v[190:191], v245, s[100:101] offset:1536
	global_load_dwordx2 v[156:157], v245, s[98:99] offset:2048 nt
	global_load_dwordx2 v[160:161], v245, s[100:101] offset:2048
	global_load_dwordx2 v[158:159], v245, s[98:99] offset:2560 nt
	global_load_dwordx2 v[166:167], v245, s[100:101] offset:2560
	global_load_dwordx2 v[162:163], v245, s[98:99] offset:3072 nt
	global_load_dwordx2 v[170:171], v245, s[100:101] offset:3072
	global_load_dwordx2 v[168:169], v245, s[98:99] offset:3584 nt
	s_waitcnt vmcnt(17)
	v_mov_b64_e32 v[174:175], v[224:225]
	v_mov_b64_e32 v[192:193], v[226:227]
	v_mov_b64_e32 v[196:197], v[246:247]
	v_mov_b64_e32 v[194:195], v[248:249]
	v_mov_b64_e32 v[200:201], v[250:251]
	v_mov_b64_e32 v[198:199], v[252:253]
	s_branch .LBB0_745
.Ln2pf_full:
	v_add_co_u32_e32 v156, vcc, 0x40100000, v164
	s_nop 1
	v_addc_co_u32_e32 v157, vcc, 0, v165, vcc
	global_load_dwordx2 v[174:175], v[156:157], off nt
	v_lshl_add_u64 v[172:173], v[152:153], 0, s[20:21]
	s_cbranch_execnz .LBB0_700

.LBB0_745:
	v_add_co_u32_e32 v172, vcc, 0x6801000, v164
	s_waitcnt vmcnt(15)
	v_cvt_f32_f16_sdwa v227, v175 dst_sel:DWORD dst_unused:UNUSED_PAD src0_sel:WORD_1
	v_cvt_f32_f16_sdwa v247, v174 dst_sel:DWORD dst_unused:UNUSED_PAD src0_sel:WORD_1
	v_cvt_f32_f16_e32 v246, v174
	v_cvt_f32_f16_e32 v226, v175
	v_addc_co_u32_e32 v173, vcc, 0, v165, vcc
	s_waitcnt vmcnt(14)
	v_lshlrev_b32_e32 v224, 16, v212
	v_and_b32_e32 v225, 0xffff0000, v212
	v_add_co_u32_e32 v212, vcc, s74, v164
	v_lshlrev_b32_e32 v174, 16, v213
	v_and_b32_e32 v175, 0xffff0000, v213
	v_addc_co_u32_e32 v213, vcc, 0, v165, vcc
	s_mov_b32 s8, 0x40101000
	v_pk_fma_f32 v[224:225], v[16:17], v[224:225], v[246:247]
	v_pk_fma_f32 v[174:175], v[18:19], v[174:175], v[226:227]
	v_add_co_u32_e32 v164, vcc, s8, v164
	v_cvt_pk_f16_f32 v227, v174, v175
	v_cvt_pk_f16_f32 v226, v224, v225
	v_addc_co_u32_e32 v165, vcc, 0, v165, vcc
	global_store_dwordx2 v[164:165], v[226:227], off offset:-4096 nt
	v_pk_mul_f32 v[226:227], v[174:175], v[174:175]
	v_pk_mul_f32 v[246:247], v[224:225], v[224:225]
	v_cvt_f32_f16_sdwa v251, v208 dst_sel:DWORD dst_unused:UNUSED_PAD src0_sel:WORD_1
	v_pk_mov_b32 v[248:249], v[246:247], v[226:227] op_sel:[1,0]
	v_mov_b32_e32 v247, v227
	v_pk_add_f32 v[226:227], v[248:249], v[246:247]
	v_cvt_f32_f16_sdwa v249, v209 dst_sel:DWORD dst_unused:UNUSED_PAD src0_sel:WORD_1
	v_cvt_f32_f16_e32 v250, v208
	v_cvt_f32_f16_e32 v248, v209
	s_waitcnt vmcnt(14)
	v_lshlrev_b32_e32 v246, 16, v214
	v_and_b32_e32 v247, 0xffff0000, v214
	v_lshlrev_b32_e32 v208, 16, v215
	v_and_b32_e32 v209, 0xffff0000, v215
	v_pk_fma_f32 v[214:215], v[0:1], v[246:247], v[250:251]
	v_pk_fma_f32 v[208:209], v[2:3], v[208:209], v[248:249]
	v_cvt_pk_f16_f32 v246, v214, v215
	v_cvt_pk_f16_f32 v247, v208, v209
	global_store_dwordx2 v[212:213], v[246:247], off offset:512 nt
	v_pk_mul_f32 v[246:247], v[208:209], v[208:209]
	v_pk_mul_f32 v[248:249], v[214:215], v[214:215]
	v_cvt_f32_f16_sdwa v253, v210 dst_sel:DWORD dst_unused:UNUSED_PAD src0_sel:WORD_1
	v_pk_mov_b32 v[250:251], v[248:249], v[246:247] op_sel:[1,0]
	v_mov_b32_e32 v249, v247
	v_pk_add_f32 v[246:247], v[250:251], v[248:249]
	v_cvt_f32_f16_sdwa v251, v211 dst_sel:DWORD dst_unused:UNUSED_PAD src0_sel:WORD_1
	v_cvt_f32_f16_e32 v250, v211
	v_cvt_f32_f16_e32 v252, v210
	s_waitcnt vmcnt(14)
	v_lshlrev_b32_e32 v210, 16, v219
	v_and_b32_e32 v211, 0xffff0000, v219
	v_lshlrev_b32_e32 v248, 16, v218
	v_and_b32_e32 v249, 0xffff0000, v218
	v_pk_fma_f32 v[210:211], v[26:27], v[210:211], v[250:251]
	v_cvt_f32_f16_sdwa v251, v216 dst_sel:DWORD dst_unused:UNUSED_PAD src0_sel:WORD_1
	v_cvt_f32_f16_e32 v250, v216
	v_pk_fma_f32 v[218:219], v[24:25], v[248:249], v[252:253]
	v_cvt_pk_f16_f32 v249, v210, v211
	v_cvt_pk_f16_f32 v248, v218, v219
	global_store_dwordx2 v[212:213], v[248:249], off offset:1024 nt
	s_waitcnt vmcnt(14)
	v_lshlrev_b32_e32 v248, 16, v220
	v_and_b32_e32 v249, 0xffff0000, v220
	v_cvt_f32_f16_sdwa v253, v217 dst_sel:DWORD dst_unused:UNUSED_PAD src0_sel:WORD_1
	v_cvt_f32_f16_e32 v252, v217
	v_lshlrev_b32_e32 v216, 16, v221
	v_and_b32_e32 v217, 0xffff0000, v221
	v_pk_fma_f32 v[220:221], v[28:29], v[248:249], v[250:251]
	v_pk_add_f32 v[226:227], v[226:227], v[226:227] op_sel:[0,1] op_sel_hi:[1,0]
	v_mul_f32_e32 v64, v220, v220
	v_mul_f32_e32 v223, v221, v221
	v_pk_add_f32 v[246:247], v[246:247], v[246:247] op_sel:[0,1] op_sel_hi:[1,0]
	v_mov_b32_e32 v227, v64
	v_mov_b32_e32 v247, v223
	v_mul_f32_e32 v64, v219, v219
	v_pk_fma_f32 v[216:217], v[30:31], v[216:217], v[252:253]
	v_pk_add_f32 v[226:227], v[226:227], v[246:247]
	v_pk_fma_f32 v[246:247], v[218:219], v[218:219], v[64:65] op_sel_hi:[1,1,0]
	v_mul_f32_e32 v64, v211, v211
	v_mul_f32_e32 v245, v216, v216
	v_mul_f32_e32 v248, v217, v217
	v_pk_fma_f32 v[250:251], v[210:211], v[210:211], v[64:65] op_sel_hi:[1,1,0]
	v_mov_b32_e32 v247, v245
	v_mov_b32_e32 v251, v248
	v_pk_add_f32 v[246:247], v[246:247], v[250:251]
	v_cvt_pk_f16_f32 v249, v216, v217
	v_pk_add_f32 v[226:227], v[226:227], v[246:247]
	v_cvt_pk_f16_f32 v248, v220, v221
	v_add_f32_e32 v64, v226, v227
	global_store_dwordx2 v[212:213], v[248:249], off offset:1536 nt
	v_mov_b32_e32 v223, v65
	v_add_f32_dpp v64, v64, v64 quad_perm:[1,0,3,2] row_mask:0xf bank_mask:0xf bound_ctrl:1
	v_lshl_add_u64 v[246:247], s[42:43], 0, v[150:151]
	global_load_dwordx2 v[172:173], v[172:173], off offset:3584
	v_add_f32_dpp v64, v64, v64 quad_perm:[2,3,0,1] row_mask:0xf bank_mask:0xf bound_ctrl:1
	v_mov_b32_e32 v245, v65
	s_nop 0
	v_add_f32_dpp v64, v64, v64 row_half_mirror row_mask:0xf bank_mask:0xf bound_ctrl:1
	s_nop 1
	v_add_f32_dpp v64, v64, v64 row_mirror row_mask:0xf bank_mask:0xf bound_ctrl:1
	s_nop 0
	v_readlane_b32 s10, v64, 16
	v_readlane_b32 s11, v64, 48
	v_readlane_b32 s8, v64, 0
	v_readlane_b32 s9, v64, 32
	v_mov_b32_e32 v226, s10
	v_mov_b32_e32 v227, s11
	v_pk_add_f32 v[226:227], s[8:9], v[226:227]
	s_mov_b32 s8, 0x36800000
	v_add_f32_e32 v64, v226, v227
	v_fmamk_f32 v64, v64, 0x3a800000, v229
	v_rsq_f32_e32 v226, v64
	s_nop 0
	v_pk_mul_f32 v[224:225], v[224:225], v[226:227] op_sel_hi:[1,0]
	v_pk_mul_f32 v[174:175], v[174:175], v[226:227] op_sel_hi:[1,0]
	v_pk_fma_f32 v[224:225], v[134:135], v[224:225], v[4:5]
	v_pk_fma_f32 v[248:249], v[132:133], v[174:175], v[6:7]
	v_med3_f32 v64, v224, s55, v228
	v_med3_f32 v174, v225, s55, v228
	v_cvt_pk_fp8_f32 v223, v64, v174
	v_med3_f32 v64, v248, s55, v228
	v_med3_f32 v174, v249, s55, v228
	v_cvt_pk_bf16_f32 v250, v224, v225
	v_cvt_pk_fp8_f32 v223, v64, v174 op_sel:[0,0,1]
	v_add_co_u32_e32 v174, vcc, s8, v246
	v_cvt_pk_bf16_f32 v251, v248, v249
	s_nop 0
	v_addc_co_u32_e32 v175, vcc, 0, v247, vcc
	v_lshlrev_b32_e32 v246, 16, v250
	v_and_b32_e32 v247, 0xffff0000, v250
	v_pk_add_f32 v[224:225], v[224:225], v[246:247] neg_lo:[0,1] neg_hi:[0,1]
	v_lshlrev_b32_e32 v246, 16, v251
	v_and_b32_e32 v247, 0xffff0000, v251
	v_pk_mul_f32 v[214:215], v[214:215], v[226:227] op_sel_hi:[1,0]
	v_pk_add_f32 v[246:247], v[248:249], v[246:247] neg_lo:[0,1] neg_hi:[0,1]
	v_pk_mul_f32 v[208:209], v[208:209], v[226:227] op_sel_hi:[1,0]
	v_pk_fma_f32 v[214:215], v[138:139], v[214:215], v[8:9]
	v_cvt_pk_bf16_f32 v224, v224, v225
	v_cvt_pk_bf16_f32 v225, v246, v247
	v_pk_fma_f32 v[208:209], v[136:137], v[208:209], v[10:11]
	v_cvt_pk_bf16_f32 v246, v214, v215
	global_store_dword v[174:175], v223, off
	v_med3_f32 v223, v214, s55, v228
	v_med3_f32 v227, v215, s55, v228
	v_cvt_pk_bf16_f32 v247, v208, v209
	v_lshlrev_b32_e32 v248, 16, v246
	v_and_b32_e32 v249, 0xffff0000, v246
	v_cvt_pk_fp8_f32 v245, v223, v227
	v_pk_add_f32 v[214:215], v[214:215], v[248:249] neg_lo:[0,1] neg_hi:[0,1]
	v_lshlrev_b32_e32 v248, 16, v247
	v_and_b32_e32 v249, 0xffff0000, v247
	v_med3_f32 v223, v208, s55, v228
	v_med3_f32 v227, v209, s55, v228
	v_pk_add_f32 v[208:209], v[208:209], v[248:249] neg_lo:[0,1] neg_hi:[0,1]
	v_cvt_pk_bf16_f32 v214, v214, v215
	v_cvt_pk_bf16_f32 v215, v208, v209
	v_pk_mul_f32 v[208:209], v[218:219], v[226:227] op_sel_hi:[1,0]
	v_cvt_pk_fp8_f32 v245, v223, v227 op_sel:[0,0,1]
	v_pk_fma_f32 v[208:209], v[142:143], v[208:209], v[20:21]
	v_pk_mul_f32 v[210:211], v[210:211], v[226:227] op_sel_hi:[1,0]
	v_med3_f32 v218, v208, s55, v228
	v_med3_f32 v219, v209, s55, v228
	v_mov_b32_e32 v227, v65
	v_cvt_pk_fp8_f32 v227, v218, v219
	v_pk_fma_f32 v[210:211], v[140:141], v[210:211], v[22:23]
	v_add_u32_e32 v223, s28, v131
	v_med3_f32 v218, v210, s55, v228
	v_med3_f32 v219, v211, s55, v228
	v_cvt_pk_fp8_f32 v227, v218, v219 op_sel:[0,0,1]
	ds_write2st64_b64 v223, v[224:225], v[214:215] offset1:1
	v_cvt_pk_bf16_f32 v214, v208, v209
	v_cvt_pk_bf16_f32 v215, v210, v211
	v_lshlrev_b32_e32 v218, 16, v214
	v_and_b32_e32 v219, 0xffff0000, v214
	v_pk_add_f32 v[208:209], v[208:209], v[218:219] neg_lo:[0,1] neg_hi:[0,1]
	v_lshlrev_b32_e32 v218, 16, v215
	v_and_b32_e32 v219, 0xffff0000, v215
	v_pk_add_f32 v[210:211], v[210:211], v[218:219] neg_lo:[0,1] neg_hi:[0,1]
	v_pk_mul_f32 v[218:219], v[220:221], v[226:227] op_sel_hi:[1,0]
	v_cvt_pk_bf16_f32 v208, v208, v209
	v_pk_fma_f32 v[218:219], v[146:147], v[218:219], v[12:13]
	v_mov_b32_e32 v221, v65
	v_med3_f32 v209, v218, s55, v228
	v_med3_f32 v220, v219, s55, v228
	v_cvt_pk_fp8_f32 v221, v209, v220
	v_pk_mul_f32 v[216:217], v[216:217], v[226:227] op_sel_hi:[1,0]
	v_add_u32_e32 v64, s27, v131
	v_pk_fma_f32 v[216:217], v[144:145], v[216:217], v[14:15]
	global_store_dword v[174:175], v245, off offset:256
	v_med3_f32 v209, v216, s55, v228
	v_med3_f32 v220, v217, s55, v228
	v_cvt_pk_fp8_f32 v221, v209, v220 op_sel:[0,0,1]
	v_cvt_pk_bf16_f32 v209, v210, v211
	v_cvt_pk_bf16_f32 v210, v218, v219
	v_cvt_pk_bf16_f32 v211, v216, v217
	global_store_dword v[174:175], v221, off offset:768
	v_lshlrev_b32_e32 v220, 16, v210
	v_and_b32_e32 v221, 0xffff0000, v210
	v_pk_add_f32 v[218:219], v[218:219], v[220:221] neg_lo:[0,1] neg_hi:[0,1]
	v_lshlrev_b32_e32 v220, 16, v211
	v_and_b32_e32 v221, 0xffff0000, v211
	v_pk_add_f32 v[216:217], v[216:217], v[220:221] neg_lo:[0,1] neg_hi:[0,1]
	ds_write2st64_b64 v64, v[250:251], v[246:247] offset1:1
	global_store_dword v[174:175], v227, off offset:512
	v_cvt_pk_bf16_f32 v218, v218, v219
	v_cvt_pk_bf16_f32 v219, v216, v217
	ds_write2st64_b64 v64, v[214:215], v[210:211] offset0:2 offset1:3
	ds_write2st64_b64 v223, v[208:209], v[218:219] offset0:2 offset1:3
	v_cvt_f32_f16_sdwa v211, v193 dst_sel:DWORD dst_unused:UNUSED_PAD src0_sel:WORD_1
	v_cvt_f32_f16_sdwa v215, v192 dst_sel:DWORD dst_unused:UNUSED_PAD src0_sel:WORD_1
	v_cvt_f32_f16_e32 v214, v192
	v_cvt_f32_f16_e32 v210, v193
	s_waitcnt vmcnt(19)
	v_lshlrev_b32_e32 v208, 16, v196
	v_and_b32_e32 v209, 0xffff0000, v196
	v_lshlrev_b32_e32 v192, 16, v197
	v_and_b32_e32 v193, 0xffff0000, v197
	v_pk_fma_f32 v[196:197], v[16:17], v[208:209], v[214:215]
	v_pk_fma_f32 v[192:193], v[18:19], v[192:193], v[210:211]
	v_cvt_pk_f16_f32 v208, v196, v197
	v_cvt_pk_f16_f32 v209, v192, v193
	global_store_dwordx2 v[212:213], v[208:209], off offset:2048 nt
	v_pk_mul_f32 v[208:209], v[192:193], v[192:193]
	v_pk_mul_f32 v[210:211], v[196:197], v[196:197]
	v_cvt_f32_f16_sdwa v217, v194 dst_sel:DWORD dst_unused:UNUSED_PAD src0_sel:WORD_1
	v_pk_mov_b32 v[214:215], v[210:211], v[208:209] op_sel:[1,0]
	v_mov_b32_e32 v211, v209
	v_pk_add_f32 v[208:209], v[214:215], v[210:211]
	v_cvt_f32_f16_sdwa v215, v195 dst_sel:DWORD dst_unused:UNUSED_PAD src0_sel:WORD_1
	v_cvt_f32_f16_e32 v216, v194
	v_cvt_f32_f16_e32 v214, v195
	s_waitcnt vmcnt(19)
	v_lshlrev_b32_e32 v210, 16, v200
	v_and_b32_e32 v211, 0xffff0000, v200
	v_lshlrev_b32_e32 v194, 16, v201
	v_and_b32_e32 v195, 0xffff0000, v201
	v_pk_fma_f32 v[200:201], v[0:1], v[210:211], v[216:217]
	v_pk_fma_f32 v[194:195], v[2:3], v[194:195], v[214:215]
	v_cvt_pk_f16_f32 v210, v200, v201
	v_cvt_pk_f16_f32 v211, v194, v195
	v_cvt_f32_f16_sdwa v219, v198 dst_sel:DWORD dst_unused:UNUSED_PAD src0_sel:WORD_1
	v_cvt_f32_f16_e32 v218, v198
	global_store_dwordx2 v[212:213], v[210:211], off offset:2560 nt
	v_pk_mul_f32 v[210:211], v[194:195], v[194:195]
	v_pk_mul_f32 v[214:215], v[200:201], v[200:201]
	s_waitcnt vmcnt(19)
	v_lshlrev_b32_e32 v198, 16, v205
	v_pk_mov_b32 v[216:217], v[214:215], v[210:211] op_sel:[1,0]
	v_mov_b32_e32 v215, v211
	v_pk_add_f32 v[210:211], v[216:217], v[214:215]
	v_lshlrev_b32_e32 v214, 16, v204
	v_and_b32_e32 v215, 0xffff0000, v204
	v_cvt_f32_f16_sdwa v217, v199 dst_sel:DWORD dst_unused:UNUSED_PAD src0_sel:WORD_1
	v_cvt_f32_f16_e32 v216, v199
	v_and_b32_e32 v199, 0xffff0000, v205
	v_pk_fma_f32 v[204:205], v[24:25], v[214:215], v[218:219]
	v_cvt_f32_f16_sdwa v219, v202 dst_sel:DWORD dst_unused:UNUSED_PAD src0_sel:WORD_1
	v_cvt_f32_f16_e32 v218, v202
	v_pk_fma_f32 v[198:199], v[26:27], v[198:199], v[216:217]
	s_waitcnt vmcnt(18)
	v_lshlrev_b32_e32 v216, 16, v206
	v_and_b32_e32 v217, 0xffff0000, v206
	v_cvt_f32_f16_sdwa v221, v203 dst_sel:DWORD dst_unused:UNUSED_PAD src0_sel:WORD_1
	v_cvt_f32_f16_e32 v220, v203
	v_lshlrev_b32_e32 v202, 16, v207
	v_and_b32_e32 v203, 0xffff0000, v207
	v_pk_fma_f32 v[206:207], v[28:29], v[216:217], v[218:219]
	v_pk_add_f32 v[208:209], v[208:209], v[208:209] op_sel:[0,1] op_sel_hi:[1,0]
	v_mul_f32_e32 v216, v206, v206
	v_mul_f32_e32 v217, v207, v207
	v_pk_add_f32 v[210:211], v[210:211], v[210:211] op_sel:[0,1] op_sel_hi:[1,0]
	v_mov_b32_e32 v209, v216
	v_mov_b32_e32 v211, v217
	v_pk_fma_f32 v[202:203], v[30:31], v[202:203], v[220:221]
	v_pk_add_f32 v[208:209], v[208:209], v[210:211]
	v_mul_f32_e32 v210, v205, v205
	v_mul_f32_e32 v216, v199, v199
	v_mul_f32_e32 v218, v202, v202
	v_mul_f32_e32 v219, v203, v203
	v_pk_fma_f32 v[210:211], v[204:205], v[204:205], v[210:211] op_sel_hi:[1,1,0]
	v_pk_fma_f32 v[216:217], v[198:199], v[198:199], v[216:217] op_sel_hi:[1,1,0]
	v_mov_b32_e32 v211, v218
	v_mov_b32_e32 v217, v219
	v_pk_add_f32 v[210:211], v[210:211], v[216:217]
	v_cvt_pk_f16_f32 v215, v198, v199
	v_pk_add_f32 v[208:209], v[208:209], v[210:211]
	v_cvt_pk_f16_f32 v214, v204, v205
	v_add_f32_e32 v208, v208, v209
	global_store_dwordx2 v[212:213], v[214:215], off offset:3072 nt
	v_mov_b32_e32 v215, v65
	v_add_f32_dpp v208, v208, v208 quad_perm:[1,0,3,2] row_mask:0xf bank_mask:0xf bound_ctrl:1
	v_cvt_pk_f16_f32 v211, v202, v203
	v_cvt_pk_f16_f32 v210, v206, v207
	v_add_f32_dpp v208, v208, v208 quad_perm:[2,3,0,1] row_mask:0xf bank_mask:0xf bound_ctrl:1
	global_store_dwordx2 v[212:213], v[210:211], off offset:3584 nt
	s_nop 0
	v_add_f32_dpp v208, v208, v208 row_half_mirror row_mask:0xf bank_mask:0xf bound_ctrl:1
	s_nop 1
	v_add_f32_dpp v208, v208, v208 row_mirror row_mask:0xf bank_mask:0xf bound_ctrl:1
	s_nop 0
	v_readlane_b32 s10, v208, 16
	v_readlane_b32 s11, v208, 48
	v_readlane_b32 s8, v208, 0
	v_readlane_b32 s9, v208, 32
	v_mov_b32_e32 v208, s10
	v_mov_b32_e32 v209, s11
	v_pk_add_f32 v[208:209], s[8:9], v[208:209]
	s_nop 0
	v_add_f32_e32 v208, v208, v209
	v_fmamk_f32 v208, v208, 0x3a800000, v229
	v_rsq_f32_e32 v208, v208
	s_nop 0
	v_pk_mul_f32 v[196:197], v[196:197], v[208:209] op_sel_hi:[1,0]
	s_nop 0
	v_pk_fma_f32 v[196:197], v[134:135], v[196:197], v[4:5]
	v_pk_mul_f32 v[192:193], v[192:193], v[208:209] op_sel_hi:[1,0]
	v_med3_f32 v209, v196, s55, v228
	v_med3_f32 v214, v197, s55, v228
	v_cvt_pk_fp8_f32 v215, v209, v214
	v_pk_fma_f32 v[192:193], v[132:133], v[192:193], v[6:7]
	v_cvt_pk_bf16_f32 v210, v196, v197
	v_cvt_pk_bf16_f32 v211, v192, v193
	v_lshlrev_b32_e32 v212, 16, v210
	v_and_b32_e32 v213, 0xffff0000, v210
	v_med3_f32 v209, v192, s55, v228
	v_med3_f32 v214, v193, s55, v228
	v_pk_add_f32 v[196:197], v[196:197], v[212:213] neg_lo:[0,1] neg_hi:[0,1]
	v_lshlrev_b32_e32 v212, 16, v211
	v_and_b32_e32 v213, 0xffff0000, v211
	v_cvt_pk_fp8_f32 v215, v209, v214 op_sel:[0,0,1]
	v_pk_add_f32 v[192:193], v[192:193], v[212:213] neg_lo:[0,1] neg_hi:[0,1]
	v_add_u32_e32 v209, s24, v236
	v_cvt_pk_bf16_f32 v196, v196, v197
	v_cvt_pk_bf16_f32 v197, v192, v193
	v_pk_mul_f32 v[192:193], v[200:201], v[208:209] op_sel_hi:[1,0]
	v_mov_b32_e32 v212, v65
	v_pk_fma_f32 v[192:193], v[138:139], v[192:193], v[8:9]
	v_pk_mul_f32 v[194:195], v[194:195], v[208:209] op_sel_hi:[1,0]
	v_med3_f32 v200, v192, s55, v228
	v_med3_f32 v201, v193, s55, v228
	v_cvt_pk_fp8_f32 v212, v200, v201
	v_pk_fma_f32 v[194:195], v[136:137], v[194:195], v[10:11]
	ds_write_b64 v209, v[196:197]
	v_med3_f32 v200, v194, s55, v228
	v_med3_f32 v201, v195, s55, v228
	v_cvt_pk_bf16_f32 v196, v192, v193
	v_cvt_pk_fp8_f32 v212, v200, v201 op_sel:[0,0,1]
	v_cvt_pk_bf16_f32 v197, v194, v195
	v_lshlrev_b32_e32 v200, 16, v196
	v_and_b32_e32 v201, 0xffff0000, v196
	v_pk_add_f32 v[192:193], v[192:193], v[200:201] neg_lo:[0,1] neg_hi:[0,1]
	v_lshlrev_b32_e32 v200, 16, v197
	v_and_b32_e32 v201, 0xffff0000, v197
	v_pk_add_f32 v[194:195], v[194:195], v[200:201] neg_lo:[0,1] neg_hi:[0,1]
	v_add_u32_e32 v209, 16, v64
	v_cvt_pk_bf16_f32 v192, v192, v193
	v_cvt_pk_bf16_f32 v193, v194, v195
	v_pk_mul_f32 v[194:195], v[204:205], v[208:209] op_sel_hi:[1,0]
	ds_write2st64_b64 v209, v[210:211], v[196:197] offset0:4 offset1:5
	v_pk_fma_f32 v[194:195], v[142:143], v[194:195], v[20:21]
	v_pk_mul_f32 v[196:197], v[198:199], v[208:209] op_sel_hi:[1,0]
	v_med3_f32 v198, v194, s55, v228
	v_med3_f32 v199, v195, s55, v228
	v_mov_b32_e32 v200, v65
	v_cvt_pk_fp8_f32 v200, v198, v199
	v_pk_fma_f32 v[196:197], v[140:141], v[196:197], v[22:23]
	v_mov_b32_e32 v205, v65
	v_med3_f32 v198, v196, s55, v228
	v_med3_f32 v199, v197, s55, v228
	v_cvt_pk_fp8_f32 v200, v198, v199 op_sel:[0,0,1]
	v_cvt_pk_bf16_f32 v198, v194, v195
	v_cvt_pk_bf16_f32 v199, v196, v197
	v_and_b32_e32 v201, 0xffff0000, v198
	global_store_dword v[174:175], v200, off offset:1536
	v_lshlrev_b32_e32 v200, 16, v198
	v_pk_add_f32 v[194:195], v[194:195], v[200:201] neg_lo:[0,1] neg_hi:[0,1]
	v_lshlrev_b32_e32 v200, 16, v199
	v_and_b32_e32 v201, 0xffff0000, v199
	v_pk_add_f32 v[196:197], v[196:197], v[200:201] neg_lo:[0,1] neg_hi:[0,1]
	v_cvt_pk_bf16_f32 v194, v194, v195
	v_cvt_pk_bf16_f32 v195, v196, v197
	v_pk_mul_f32 v[196:197], v[206:207], v[208:209] op_sel_hi:[1,0]
	v_pk_mul_f32 v[200:201], v[202:203], v[208:209] op_sel_hi:[1,0]
	v_pk_fma_f32 v[196:197], v[146:147], v[196:197], v[12:13]
	v_add_u32_e32 v204, s29, v131
	v_med3_f32 v202, v196, s55, v228
	v_med3_f32 v203, v197, s55, v228
	v_cvt_pk_fp8_f32 v205, v202, v203
	v_pk_fma_f32 v[200:201], v[144:145], v[200:201], v[14:15]
	ds_write2st64_b64 v204, v[192:193], v[194:195] offset0:1 offset1:2
	v_med3_f32 v202, v200, s55, v228
	v_med3_f32 v203, v201, s55, v228
	v_cvt_pk_bf16_f32 v192, v196, v197
	v_cvt_pk_fp8_f32 v205, v202, v203 op_sel:[0,0,1]
	v_cvt_pk_bf16_f32 v193, v200, v201
	v_lshlrev_b32_e32 v194, 16, v192
	v_and_b32_e32 v195, 0xffff0000, v192
	v_pk_add_f32 v[194:195], v[196:197], v[194:195] neg_lo:[0,1] neg_hi:[0,1]
	v_lshlrev_b32_e32 v196, 16, v193
	v_and_b32_e32 v197, 0xffff0000, v193
	v_pk_add_f32 v[196:197], v[200:201], v[196:197] neg_lo:[0,1] neg_hi:[0,1]
	v_cvt_pk_bf16_f32 v194, v194, v195
	v_cvt_pk_bf16_f32 v195, v196, v197
	global_store_dword v[174:175], v215, off offset:1024
	global_store_dword v[174:175], v212, off offset:1280
	global_store_dword v[174:175], v205, off offset:1792
	ds_write2st64_b64 v209, v[198:199], v[192:193] offset0:6 offset1:7
	ds_write_b64 v204, v[194:195] offset:1536
	v_cvt_f32_f16_sdwa v195, v177 dst_sel:DWORD dst_unused:UNUSED_PAD src0_sel:WORD_1
	v_cvt_f32_f16_sdwa v197, v176 dst_sel:DWORD dst_unused:UNUSED_PAD src0_sel:WORD_1
	v_cvt_f32_f16_e32 v196, v176
	v_cvt_f32_f16_e32 v194, v177
	s_waitcnt vmcnt(23)
	v_lshlrev_b32_e32 v192, 16, v180
	v_and_b32_e32 v193, 0xffff0000, v180
	v_lshlrev_b32_e32 v176, 16, v181
	v_and_b32_e32 v177, 0xffff0000, v181
	v_pk_fma_f32 v[180:181], v[16:17], v[192:193], v[196:197]
	v_pk_fma_f32 v[176:177], v[18:19], v[176:177], v[194:195]
	v_cvt_pk_f16_f32 v192, v180, v181
	v_cvt_pk_f16_f32 v193, v176, v177
	global_store_dwordx2 v[164:165], v[192:193], off nt
	v_pk_mul_f32 v[192:193], v[176:177], v[176:177]
	v_pk_mul_f32 v[194:195], v[180:181], v[180:181]
	v_cvt_f32_f16_sdwa v199, v178 dst_sel:DWORD dst_unused:UNUSED_PAD src0_sel:WORD_1
	v_pk_mov_b32 v[196:197], v[194:195], v[192:193] op_sel:[1,0]
	v_mov_b32_e32 v195, v193
	v_pk_add_f32 v[192:193], v[196:197], v[194:195]
	v_cvt_f32_f16_sdwa v197, v179 dst_sel:DWORD dst_unused:UNUSED_PAD src0_sel:WORD_1
	v_cvt_f32_f16_e32 v198, v178
	v_cvt_f32_f16_e32 v196, v179
	s_waitcnt vmcnt(23)
	v_lshlrev_b32_e32 v194, 16, v184
	v_and_b32_e32 v195, 0xffff0000, v184
	v_lshlrev_b32_e32 v178, 16, v185
	v_and_b32_e32 v179, 0xffff0000, v185
	v_pk_fma_f32 v[184:185], v[0:1], v[194:195], v[198:199]
	v_pk_fma_f32 v[178:179], v[2:3], v[178:179], v[196:197]
	v_cvt_pk_f16_f32 v194, v184, v185
	v_cvt_pk_f16_f32 v195, v178, v179
	v_cvt_f32_f16_sdwa v201, v182 dst_sel:DWORD dst_unused:UNUSED_PAD src0_sel:WORD_1
	v_cvt_f32_f16_e32 v200, v182
	global_store_dwordx2 v[164:165], v[194:195], off offset:512 nt
	v_pk_mul_f32 v[194:195], v[178:179], v[178:179]
	v_pk_mul_f32 v[196:197], v[184:185], v[184:185]
	s_waitcnt vmcnt(23)
	v_lshlrev_b32_e32 v182, 16, v189
	v_pk_mov_b32 v[198:199], v[196:197], v[194:195] op_sel:[1,0]
	v_mov_b32_e32 v197, v195
	v_pk_add_f32 v[194:195], v[198:199], v[196:197]
	v_lshlrev_b32_e32 v196, 16, v188
	v_and_b32_e32 v197, 0xffff0000, v188
	v_cvt_f32_f16_sdwa v199, v183 dst_sel:DWORD dst_unused:UNUSED_PAD src0_sel:WORD_1
	v_cvt_f32_f16_e32 v198, v183
	v_and_b32_e32 v183, 0xffff0000, v189
	v_pk_fma_f32 v[188:189], v[24:25], v[196:197], v[200:201]
	v_cvt_f32_f16_sdwa v201, v186 dst_sel:DWORD dst_unused:UNUSED_PAD src0_sel:WORD_1
	v_cvt_f32_f16_e32 v200, v186
	v_pk_fma_f32 v[182:183], v[26:27], v[182:183], v[198:199]
	s_waitcnt vmcnt(22)
	v_lshlrev_b32_e32 v198, 16, v190
	v_and_b32_e32 v199, 0xffff0000, v190
	v_cvt_f32_f16_sdwa v203, v187 dst_sel:DWORD dst_unused:UNUSED_PAD src0_sel:WORD_1
	v_cvt_f32_f16_e32 v202, v187
	v_lshlrev_b32_e32 v186, 16, v191
	v_and_b32_e32 v187, 0xffff0000, v191
	v_pk_fma_f32 v[190:191], v[28:29], v[198:199], v[200:201]
	v_pk_add_f32 v[192:193], v[192:193], v[192:193] op_sel:[0,1] op_sel_hi:[1,0]
	v_mul_f32_e32 v198, v190, v190
	v_mul_f32_e32 v199, v191, v191
	v_pk_add_f32 v[194:195], v[194:195], v[194:195] op_sel:[0,1] op_sel_hi:[1,0]
	v_mov_b32_e32 v193, v198
	v_mov_b32_e32 v195, v199
	v_pk_fma_f32 v[186:187], v[30:31], v[186:187], v[202:203]
	v_pk_add_f32 v[192:193], v[192:193], v[194:195]
	v_mul_f32_e32 v194, v189, v189
	v_mul_f32_e32 v198, v183, v183
	v_mul_f32_e32 v200, v186, v186
	v_mul_f32_e32 v201, v187, v187
	v_pk_fma_f32 v[194:195], v[188:189], v[188:189], v[194:195] op_sel_hi:[1,1,0]
	v_pk_fma_f32 v[198:199], v[182:183], v[182:183], v[198:199] op_sel_hi:[1,1,0]
	v_mov_b32_e32 v195, v200
	v_mov_b32_e32 v199, v201
	v_pk_add_f32 v[194:195], v[194:195], v[198:199]
	v_cvt_pk_f16_f32 v197, v182, v183
	v_pk_add_f32 v[192:193], v[192:193], v[194:195]
	v_cvt_pk_f16_f32 v196, v188, v189
	v_add_f32_e32 v192, v192, v193
	global_store_dwordx2 v[164:165], v[196:197], off offset:1024 nt
	v_mov_b32_e32 v197, v65
	v_add_f32_dpp v192, v192, v192 quad_perm:[1,0,3,2] row_mask:0xf bank_mask:0xf bound_ctrl:1
	v_cvt_pk_f16_f32 v195, v186, v187
	v_cvt_pk_f16_f32 v194, v190, v191
	v_add_f32_dpp v192, v192, v192 quad_perm:[2,3,0,1] row_mask:0xf bank_mask:0xf bound_ctrl:1
	global_store_dwordx2 v[164:165], v[194:195], off offset:1536 nt
	s_nop 0
	v_add_f32_dpp v192, v192, v192 row_half_mirror row_mask:0xf bank_mask:0xf bound_ctrl:1
	s_nop 1
	v_add_f32_dpp v192, v192, v192 row_mirror row_mask:0xf bank_mask:0xf bound_ctrl:1
	s_nop 0
	v_readlane_b32 s10, v192, 16
	v_readlane_b32 s11, v192, 48
	v_readlane_b32 s8, v192, 0
	v_readlane_b32 s9, v192, 32
	v_mov_b32_e32 v192, s10
	v_mov_b32_e32 v193, s11
	v_pk_add_f32 v[192:193], s[8:9], v[192:193]
	s_nop 0
	v_add_f32_e32 v192, v192, v193
	v_fmamk_f32 v192, v192, 0x3a800000, v229
	v_rsq_f32_e32 v192, v192
	s_nop 0
	v_pk_mul_f32 v[180:181], v[180:181], v[192:193] op_sel_hi:[1,0]
	s_nop 0
	v_pk_fma_f32 v[180:181], v[134:135], v[180:181], v[4:5]
	v_pk_mul_f32 v[176:177], v[176:177], v[192:193] op_sel_hi:[1,0]
	v_med3_f32 v193, v180, s55, v228
	v_med3_f32 v196, v181, s55, v228
	v_cvt_pk_fp8_f32 v197, v193, v196
	v_pk_fma_f32 v[176:177], v[132:133], v[176:177], v[6:7]
	v_cvt_pk_bf16_f32 v194, v180, v181
	v_med3_f32 v193, v176, s55, v228
	v_med3_f32 v196, v177, s55, v228
	v_cvt_pk_fp8_f32 v197, v193, v196 op_sel:[0,0,1]
	v_cvt_pk_bf16_f32 v195, v176, v177
	v_lshlrev_b32_e32 v196, 16, v194
	v_add_u32_e32 v193, s25, v236
	global_store_dword v[174:175], v197, off offset:2048
	v_and_b32_e32 v197, 0xffff0000, v194
	v_pk_add_f32 v[180:181], v[180:181], v[196:197] neg_lo:[0,1] neg_hi:[0,1]
	v_lshlrev_b32_e32 v196, 16, v195
	v_and_b32_e32 v197, 0xffff0000, v195
	v_pk_add_f32 v[176:177], v[176:177], v[196:197] neg_lo:[0,1] neg_hi:[0,1]
	v_cvt_pk_bf16_f32 v180, v180, v181
	v_cvt_pk_bf16_f32 v181, v176, v177
	v_pk_mul_f32 v[176:177], v[184:185], v[192:193] op_sel_hi:[1,0]
	v_mov_b32_e32 v196, v65
	v_pk_fma_f32 v[176:177], v[138:139], v[176:177], v[8:9]
	v_pk_mul_f32 v[178:179], v[178:179], v[192:193] op_sel_hi:[1,0]
	v_med3_f32 v184, v176, s55, v228
	v_med3_f32 v185, v177, s55, v228
	v_cvt_pk_fp8_f32 v196, v184, v185
	v_pk_fma_f32 v[178:179], v[136:137], v[178:179], v[10:11]
	ds_write_b64 v193, v[180:181]
	v_med3_f32 v184, v178, s55, v228
	v_med3_f32 v185, v179, s55, v228
	v_cvt_pk_bf16_f32 v180, v176, v177
	v_cvt_pk_fp8_f32 v196, v184, v185 op_sel:[0,0,1]
	v_cvt_pk_bf16_f32 v181, v178, v179
	v_lshlrev_b32_e32 v184, 16, v180
	v_and_b32_e32 v185, 0xffff0000, v180
	v_pk_add_f32 v[176:177], v[176:177], v[184:185] neg_lo:[0,1] neg_hi:[0,1]
	v_lshlrev_b32_e32 v184, 16, v181
	v_and_b32_e32 v185, 0xffff0000, v181
	v_pk_add_f32 v[178:179], v[178:179], v[184:185] neg_lo:[0,1] neg_hi:[0,1]
	v_add_u32_e32 v193, 32, v64
	v_cvt_pk_bf16_f32 v176, v176, v177
	v_cvt_pk_bf16_f32 v177, v178, v179
	v_pk_mul_f32 v[178:179], v[188:189], v[192:193] op_sel_hi:[1,0]
	ds_write2st64_b64 v193, v[194:195], v[180:181] offset0:8 offset1:9
	v_pk_fma_f32 v[178:179], v[142:143], v[178:179], v[20:21]
	v_pk_mul_f32 v[180:181], v[182:183], v[192:193] op_sel_hi:[1,0]
	v_med3_f32 v182, v178, s55, v228
	v_med3_f32 v183, v179, s55, v228
	v_mov_b32_e32 v184, v65
	v_cvt_pk_fp8_f32 v184, v182, v183
	v_pk_fma_f32 v[180:181], v[140:141], v[180:181], v[22:23]
	v_mov_b32_e32 v189, v65
	v_med3_f32 v182, v180, s55, v228
	v_med3_f32 v183, v181, s55, v228
	v_cvt_pk_fp8_f32 v184, v182, v183 op_sel:[0,0,1]
	v_cvt_pk_bf16_f32 v182, v178, v179
	v_cvt_pk_bf16_f32 v183, v180, v181
	v_and_b32_e32 v185, 0xffff0000, v182
	global_store_dword v[174:175], v184, off offset:2560
	v_lshlrev_b32_e32 v184, 16, v182
	v_pk_add_f32 v[178:179], v[178:179], v[184:185] neg_lo:[0,1] neg_hi:[0,1]
	v_lshlrev_b32_e32 v184, 16, v183
	v_and_b32_e32 v185, 0xffff0000, v183
	v_pk_add_f32 v[180:181], v[180:181], v[184:185] neg_lo:[0,1] neg_hi:[0,1]
	v_cvt_pk_bf16_f32 v178, v178, v179
	v_cvt_pk_bf16_f32 v179, v180, v181
	v_pk_mul_f32 v[180:181], v[190:191], v[192:193] op_sel_hi:[1,0]
	v_pk_mul_f32 v[184:185], v[186:187], v[192:193] op_sel_hi:[1,0]
	v_pk_fma_f32 v[180:181], v[146:147], v[180:181], v[12:13]
	v_add_u32_e32 v188, s30, v131
	v_med3_f32 v186, v180, s55, v228
	v_med3_f32 v187, v181, s55, v228
	v_cvt_pk_fp8_f32 v189, v186, v187
	v_pk_fma_f32 v[184:185], v[144:145], v[184:185], v[14:15]
	ds_write2st64_b64 v188, v[176:177], v[178:179] offset0:1 offset1:2
	v_med3_f32 v186, v184, s55, v228
	v_med3_f32 v187, v185, s55, v228
	v_cvt_pk_bf16_f32 v176, v180, v181
	v_cvt_pk_fp8_f32 v189, v186, v187 op_sel:[0,0,1]
	v_cvt_pk_bf16_f32 v177, v184, v185
	v_lshlrev_b32_e32 v178, 16, v176
	v_and_b32_e32 v179, 0xffff0000, v176
	v_pk_add_f32 v[178:179], v[180:181], v[178:179] neg_lo:[0,1] neg_hi:[0,1]
	v_lshlrev_b32_e32 v180, 16, v177
	v_and_b32_e32 v181, 0xffff0000, v177
	v_pk_add_f32 v[180:181], v[184:185], v[180:181] neg_lo:[0,1] neg_hi:[0,1]
	v_cvt_pk_bf16_f32 v178, v178, v179
	v_cvt_pk_bf16_f32 v179, v180, v181
	global_store_dword v[174:175], v196, off offset:2304
	global_store_dword v[174:175], v189, off offset:2816
	ds_write2st64_b64 v193, v[182:183], v[176:177] offset0:10 offset1:11
	ds_write_b64 v188, v[178:179] offset:1536
	v_cvt_f32_f16_sdwa v179, v157 dst_sel:DWORD dst_unused:UNUSED_PAD src0_sel:WORD_1
	v_cvt_f32_f16_sdwa v181, v156 dst_sel:DWORD dst_unused:UNUSED_PAD src0_sel:WORD_1
	v_cvt_f32_f16_e32 v180, v156
	v_cvt_f32_f16_e32 v178, v157
	s_waitcnt vmcnt(27)
	v_lshlrev_b32_e32 v176, 16, v160
	v_and_b32_e32 v177, 0xffff0000, v160
	v_lshlrev_b32_e32 v156, 16, v161
	v_and_b32_e32 v157, 0xffff0000, v161
	v_pk_fma_f32 v[160:161], v[16:17], v[176:177], v[180:181]
	v_pk_fma_f32 v[156:157], v[18:19], v[156:157], v[178:179]
	v_cvt_pk_f16_f32 v176, v160, v161
	v_cvt_pk_f16_f32 v177, v156, v157
	global_store_dwordx2 v[164:165], v[176:177], off offset:2048 nt
	v_pk_mul_f32 v[176:177], v[156:157], v[156:157]
	v_pk_mul_f32 v[178:179], v[160:161], v[160:161]
	v_cvt_f32_f16_sdwa v183, v158 dst_sel:DWORD dst_unused:UNUSED_PAD src0_sel:WORD_1
	v_pk_mov_b32 v[180:181], v[178:179], v[176:177] op_sel:[1,0]
	v_mov_b32_e32 v179, v177
	v_pk_add_f32 v[176:177], v[180:181], v[178:179]
	v_cvt_f32_f16_sdwa v181, v159 dst_sel:DWORD dst_unused:UNUSED_PAD src0_sel:WORD_1
	v_cvt_f32_f16_e32 v182, v158
	v_cvt_f32_f16_e32 v180, v159
	s_waitcnt vmcnt(27)
	v_lshlrev_b32_e32 v178, 16, v166
	v_and_b32_e32 v179, 0xffff0000, v166
	v_lshlrev_b32_e32 v158, 16, v167
	v_and_b32_e32 v159, 0xffff0000, v167
	v_pk_fma_f32 v[166:167], v[0:1], v[178:179], v[182:183]
	v_pk_fma_f32 v[158:159], v[2:3], v[158:159], v[180:181]
	v_cvt_pk_f16_f32 v178, v166, v167
	v_cvt_pk_f16_f32 v179, v158, v159
	v_cvt_f32_f16_sdwa v185, v162 dst_sel:DWORD dst_unused:UNUSED_PAD src0_sel:WORD_1
	v_cvt_f32_f16_e32 v184, v162
	global_store_dwordx2 v[164:165], v[178:179], off offset:2560 nt
	v_pk_mul_f32 v[178:179], v[158:159], v[158:159]
	v_pk_mul_f32 v[180:181], v[166:167], v[166:167]
	s_waitcnt vmcnt(27)
	v_lshlrev_b32_e32 v162, 16, v171
	v_pk_mov_b32 v[182:183], v[180:181], v[178:179] op_sel:[1,0]
	v_mov_b32_e32 v181, v179
	v_pk_add_f32 v[178:179], v[182:183], v[180:181]
	v_lshlrev_b32_e32 v180, 16, v170
	v_and_b32_e32 v181, 0xffff0000, v170
	v_cvt_f32_f16_sdwa v183, v163 dst_sel:DWORD dst_unused:UNUSED_PAD src0_sel:WORD_1
	v_cvt_f32_f16_e32 v182, v163
	v_and_b32_e32 v163, 0xffff0000, v171
	v_pk_fma_f32 v[170:171], v[24:25], v[180:181], v[184:185]
	v_cvt_f32_f16_sdwa v185, v168 dst_sel:DWORD dst_unused:UNUSED_PAD src0_sel:WORD_1
	v_cvt_f32_f16_e32 v184, v168
	v_pk_fma_f32 v[162:163], v[26:27], v[162:163], v[182:183]
	s_waitcnt vmcnt(22)
	v_lshlrev_b32_e32 v182, 16, v172
	v_and_b32_e32 v183, 0xffff0000, v172
	v_cvt_f32_f16_sdwa v187, v169 dst_sel:DWORD dst_unused:UNUSED_PAD src0_sel:WORD_1
	v_cvt_f32_f16_e32 v186, v169
	v_lshlrev_b32_e32 v168, 16, v173
	v_and_b32_e32 v169, 0xffff0000, v173
	v_pk_fma_f32 v[172:173], v[28:29], v[182:183], v[184:185]
	v_pk_add_f32 v[176:177], v[176:177], v[176:177] op_sel:[0,1] op_sel_hi:[1,0]
	v_mul_f32_e32 v182, v172, v172
	v_mul_f32_e32 v183, v173, v173
	v_pk_add_f32 v[178:179], v[178:179], v[178:179] op_sel:[0,1] op_sel_hi:[1,0]
	v_mov_b32_e32 v177, v182
	v_mov_b32_e32 v179, v183
	v_pk_fma_f32 v[168:169], v[30:31], v[168:169], v[186:187]
	v_pk_add_f32 v[176:177], v[176:177], v[178:179]
	v_mul_f32_e32 v178, v171, v171
	v_mul_f32_e32 v182, v163, v163
	v_mul_f32_e32 v184, v168, v168
	v_mul_f32_e32 v185, v169, v169
	v_pk_fma_f32 v[178:179], v[170:171], v[170:171], v[178:179] op_sel_hi:[1,1,0]
	v_pk_fma_f32 v[182:183], v[162:163], v[162:163], v[182:183] op_sel_hi:[1,1,0]
	v_mov_b32_e32 v179, v184
	v_mov_b32_e32 v183, v185
	v_pk_add_f32 v[178:179], v[178:179], v[182:183]
	v_cvt_pk_f16_f32 v181, v162, v163
	v_pk_add_f32 v[176:177], v[176:177], v[178:179]
	v_cvt_pk_f16_f32 v180, v170, v171
	v_add_f32_e32 v176, v176, v177
	global_store_dwordx2 v[164:165], v[180:181], off offset:3072 nt
	v_mov_b32_e32 v181, v65
	v_add_f32_dpp v176, v176, v176 quad_perm:[1,0,3,2] row_mask:0xf bank_mask:0xf bound_ctrl:1
	v_cvt_pk_f16_f32 v179, v168, v169
	v_cvt_pk_f16_f32 v178, v172, v173
	v_add_f32_dpp v176, v176, v176 quad_perm:[2,3,0,1] row_mask:0xf bank_mask:0xf bound_ctrl:1
	global_store_dwordx2 v[164:165], v[178:179], off offset:3584 nt
	v_add_u32_e32 v64, 48, v64
	v_add_f32_dpp v176, v176, v176 row_half_mirror row_mask:0xf bank_mask:0xf bound_ctrl:1
	s_nop 1
	v_add_f32_dpp v176, v176, v176 row_mirror row_mask:0xf bank_mask:0xf bound_ctrl:1
	s_nop 0
	v_readlane_b32 s10, v176, 16
	v_readlane_b32 s11, v176, 48
	v_readlane_b32 s8, v176, 0
	v_readlane_b32 s9, v176, 32
	v_mov_b32_e32 v176, s10
	v_mov_b32_e32 v177, s11
	v_pk_add_f32 v[176:177], s[8:9], v[176:177]
	s_nop 0
	v_add_f32_e32 v176, v176, v177
	v_fmamk_f32 v176, v176, 0x3a800000, v229
	v_rsq_f32_e32 v176, v176
	s_nop 0
	v_pk_mul_f32 v[160:161], v[160:161], v[176:177] op_sel_hi:[1,0]
	s_nop 0
	v_pk_fma_f32 v[160:161], v[134:135], v[160:161], v[4:5]
	v_pk_mul_f32 v[156:157], v[156:157], v[176:177] op_sel_hi:[1,0]
	v_med3_f32 v177, v160, s55, v228
	v_med3_f32 v180, v161, s55, v228
	v_cvt_pk_fp8_f32 v181, v177, v180
	v_pk_fma_f32 v[156:157], v[132:133], v[156:157], v[6:7]
	v_cvt_pk_bf16_f32 v164, v160, v161
	v_cvt_pk_bf16_f32 v165, v156, v157
	v_lshlrev_b32_e32 v178, 16, v164
	v_and_b32_e32 v179, 0xffff0000, v164
	v_med3_f32 v177, v156, s55, v228
	v_med3_f32 v180, v157, s55, v228
	v_pk_add_f32 v[160:161], v[160:161], v[178:179] neg_lo:[0,1] neg_hi:[0,1]
	v_lshlrev_b32_e32 v178, 16, v165
	v_and_b32_e32 v179, 0xffff0000, v165
	v_cvt_pk_fp8_f32 v181, v177, v180 op_sel:[0,0,1]
	v_pk_add_f32 v[156:157], v[156:157], v[178:179] neg_lo:[0,1] neg_hi:[0,1]
	v_add_u32_e32 v177, s26, v236
	v_cvt_pk_bf16_f32 v160, v160, v161
	v_cvt_pk_bf16_f32 v161, v156, v157
	v_pk_mul_f32 v[156:157], v[166:167], v[176:177] op_sel_hi:[1,0]
	v_mov_b32_e32 v178, v65
	v_pk_fma_f32 v[156:157], v[138:139], v[156:157], v[8:9]
	v_pk_mul_f32 v[158:159], v[158:159], v[176:177] op_sel_hi:[1,0]
	v_med3_f32 v166, v156, s55, v228
	v_med3_f32 v167, v157, s55, v228
	v_cvt_pk_fp8_f32 v178, v166, v167
	v_pk_fma_f32 v[158:159], v[136:137], v[158:159], v[10:11]
	ds_write_b64 v177, v[160:161]
	v_med3_f32 v166, v158, s55, v228
	v_med3_f32 v167, v159, s55, v228
	v_cvt_pk_bf16_f32 v160, v156, v157
	v_cvt_pk_fp8_f32 v178, v166, v167 op_sel:[0,0,1]
	v_cvt_pk_bf16_f32 v161, v158, v159
	v_lshlrev_b32_e32 v166, 16, v160
	v_and_b32_e32 v167, 0xffff0000, v160
	v_pk_add_f32 v[156:157], v[156:157], v[166:167] neg_lo:[0,1] neg_hi:[0,1]
	v_lshlrev_b32_e32 v166, 16, v161
	v_and_b32_e32 v167, 0xffff0000, v161
	v_pk_add_f32 v[158:159], v[158:159], v[166:167] neg_lo:[0,1] neg_hi:[0,1]
	v_cvt_pk_bf16_f32 v156, v156, v157
	v_cvt_pk_bf16_f32 v157, v158, v159
	v_pk_mul_f32 v[158:159], v[170:171], v[176:177] op_sel_hi:[1,0]
	ds_write2st64_b64 v64, v[164:165], v[160:161] offset0:12 offset1:13
	v_pk_fma_f32 v[158:159], v[142:143], v[158:159], v[20:21]
	v_pk_mul_f32 v[160:161], v[162:163], v[176:177] op_sel_hi:[1,0]
	v_med3_f32 v162, v158, s55, v228
	v_med3_f32 v163, v159, s55, v228
	v_mov_b32_e32 v164, v65
	v_cvt_pk_fp8_f32 v164, v162, v163
	v_pk_fma_f32 v[160:161], v[140:141], v[160:161], v[22:23]
	v_add_u32_e32 v166, s31, v131
	v_med3_f32 v162, v160, s55, v228
	v_med3_f32 v163, v161, s55, v228
	v_cvt_pk_fp8_f32 v164, v162, v163 op_sel:[0,0,1]
	v_cvt_pk_bf16_f32 v162, v158, v159
	v_cvt_pk_bf16_f32 v163, v160, v161
	v_and_b32_e32 v165, 0xffff0000, v162
	global_store_dword v[174:175], v164, off offset:3584
	v_lshlrev_b32_e32 v164, 16, v162
	v_pk_add_f32 v[158:159], v[158:159], v[164:165] neg_lo:[0,1] neg_hi:[0,1]
	v_lshlrev_b32_e32 v164, 16, v163
	v_and_b32_e32 v165, 0xffff0000, v163
	v_pk_add_f32 v[160:161], v[160:161], v[164:165] neg_lo:[0,1] neg_hi:[0,1]
	v_cvt_pk_bf16_f32 v158, v158, v159
	v_cvt_pk_bf16_f32 v159, v160, v161
	v_pk_mul_f32 v[160:161], v[172:173], v[176:177] op_sel_hi:[1,0]
	v_pk_mul_f32 v[164:165], v[168:169], v[176:177] op_sel_hi:[1,0]
	v_pk_fma_f32 v[160:161], v[146:147], v[160:161], v[12:13]
	v_mov_b32_e32 v169, v65
	v_med3_f32 v167, v160, s55, v228
	v_med3_f32 v168, v161, s55, v228
	v_cvt_pk_fp8_f32 v169, v167, v168
	v_pk_fma_f32 v[164:165], v[144:145], v[164:165], v[14:15]
	ds_write2st64_b64 v166, v[156:157], v[158:159] offset0:1 offset1:2
	v_med3_f32 v167, v164, s55, v228
	v_med3_f32 v168, v165, s55, v228
	v_cvt_pk_fp8_f32 v169, v167, v168 op_sel:[0,0,1]
	v_cvt_pk_bf16_f32 v156, v160, v161
	v_cvt_pk_bf16_f32 v157, v164, v165
	v_lshlrev_b32_e32 v158, 16, v156
	v_and_b32_e32 v159, 0xffff0000, v156
	v_pk_add_f32 v[158:159], v[160:161], v[158:159] neg_lo:[0,1] neg_hi:[0,1]
	v_lshlrev_b32_e32 v160, 16, v157
	v_and_b32_e32 v161, 0xffff0000, v157
	v_pk_add_f32 v[160:161], v[164:165], v[160:161] neg_lo:[0,1] neg_hi:[0,1]
	global_store_dword v[174:175], v181, off offset:3072
	global_store_dword v[174:175], v178, off offset:3328
	global_store_dword v[174:175], v169, off offset:3840
	v_cvt_pk_bf16_f32 v158, v158, v159
	v_cvt_pk_bf16_f32 v159, v160, v161
	ds_write2st64_b64 v64, v[162:163], v[156:157] offset0:14 offset1:15
	ds_write_b64 v166, v[158:159] offset:1536
	v_add_u32_e32 v64, 0, v232
	s_and_b64 vcc, exec, s[86:87]
	s_cbranch_vccz .Ln2pf_skip
	s_cmp_eq_u32 s20, 0x1c000
	s_cbranch_scc1 .Ln2pf_skip
	v_add_u32_e32 v223, 0x2000, v154
	global_load_dwordx2 v[224:225], v223, s[98:99] nt
	global_load_dwordx2 v[212:213], v223, s[100:101]
	global_load_dwordx2 v[208:209], v223, s[98:99] offset:512 nt
	global_load_dwordx2 v[214:215], v223, s[100:101] offset:512
	global_load_dwordx2 v[210:211], v223, s[98:99] offset:1024 nt
	global_load_dwordx2 v[218:219], v223, s[100:101] offset:1024
	global_load_dwordx2 v[216:217], v223, s[98:99] offset:1536 nt
	global_load_dwordx2 v[220:221], v223, s[100:101] offset:1536
	global_load_dwordx2 v[226:227], v223, s[98:99] offset:2048 nt
	global_load_dwordx2 v[246:247], v223, s[100:101] offset:2048
	global_load_dwordx2 v[248:249], v223, s[98:99] offset:2560 nt
	global_load_dwordx2 v[250:251], v223, s[100:101] offset:2560
	global_load_dwordx2 v[252:253], v223, s[98:99] offset:3072 nt
	global_load_dwordx2 v[204:205], v223, s[100:101] offset:3072
.Ln2pf_skip:
	s_waitcnt lgkmcnt(0)
	s_barrier
	ds_read_b128 v[156:159], v64
	ds_read_b128 v[160:163], v64 offset:33024
	s_waitcnt lgkmcnt(1)
	v_mfma_f32_16x16x32_bf16 v[164:167], v[156:159], v[32:35], 0
	v_add_u32_e32 v168, s61, v232
	ds_read_b128 v[168:171], v168
	ds_read_b128 v[172:175], v64 offset:192
	v_mfma_f32_16x16x32_bf16 v[176:179], v[156:159], v[44:47], 0
	v_mfma_f32_16x16x32_bf16 v[180:183], v[156:159], v[40:43], 0
	v_mfma_f32_16x16x32_bf16 v[164:167], v[156:159], v[94:97], v[164:167]
	v_mfma_f32_16x16x32_bf16 v[176:179], v[156:159], v[36:39], v[176:179]
	v_mfma_f32_16x16x32_bf16 v[156:159], v[156:159], v[118:121], v[180:183]
	s_waitcnt lgkmcnt(1)
	v_mfma_f32_16x16x32_bf16 v[164:167], v[168:171], v[32:35], v[164:167]
	s_nop 2
	v_add_u32_e32 v180, s61, v233
	ds_read_b128 v[180:183], v180
	ds_read_b128 v[184:187], v239
	v_mfma_f32_16x16x32_bf16 v[176:179], v[168:171], v[44:47], v[176:179]
	v_mfma_f32_16x16x32_bf16 v[156:159], v[168:171], v[40:43], v[156:159]
	v_mfma_f32_16x16x32_bf16 v[168:171], v[160:163], v[32:35], 0
	v_mfma_f32_16x16x32_bf16 v[188:191], v[160:163], v[44:47], 0
	v_mfma_f32_16x16x32_bf16 v[192:195], v[160:163], v[40:43], 0
	v_mfma_f32_16x16x32_bf16 v[168:171], v[160:163], v[94:97], v[168:171]
	v_mfma_f32_16x16x32_bf16 v[188:191], v[160:163], v[36:39], v[188:191]
	v_mfma_f32_16x16x32_bf16 v[160:163], v[160:163], v[118:121], v[192:195]
	s_waitcnt lgkmcnt(1)
	v_mfma_f32_16x16x32_bf16 v[168:171], v[180:183], v[32:35], v[168:171]
	v_mfma_f32_16x16x32_bf16 v[188:191], v[180:183], v[44:47], v[188:191]
	v_mfma_f32_16x16x32_bf16 v[160:163], v[180:183], v[40:43], v[160:163]
	ds_read_b128 v[180:183], v64 offset:64
	ds_read_b128 v[192:195], v64 offset:128
	v_add_u32_e32 v64, 0, v233
	s_waitcnt lgkmcnt(1)
	v_mfma_f32_16x16x32_bf16 v[164:167], v[180:183], v[60:63], v[164:167]
	v_mfma_f32_16x16x32_bf16 v[176:179], v[180:183], v[48:51], v[176:179]
	v_mfma_f32_16x16x32_bf16 v[156:159], v[180:183], v[78:81], v[156:159]
	v_mfma_f32_16x16x32_bf16 v[164:167], v[180:183], v[52:55], v[164:167]
	v_mfma_f32_16x16x32_bf16 v[176:179], v[180:183], v[56:59], v[176:179]
	v_mfma_f32_16x16x32_bf16 v[156:159], v[180:183], v[70:73], v[156:159]
	v_mfma_f32_16x16x32_bf16 v[164:167], v[184:187], v[60:63], v[164:167]
	v_mfma_f32_16x16x32_bf16 v[176:179], v[184:187], v[48:51], v[176:179]
	v_mfma_f32_16x16x32_bf16 v[156:159], v[184:187], v[78:81], v[156:159]
	ds_read_b128 v[180:183], v64 offset:64
	ds_read_b128 v[184:187], v64 offset:128
	ds_read_b128 v[196:199], v240
	ds_read_b128 v[200:203], v64 offset:192
	v_add_u32_e32 v64, 0xc00, v238
	s_waitcnt lgkmcnt(3)
	v_mfma_f32_16x16x32_bf16 v[168:171], v[180:183], v[60:63], v[168:171]
	v_mfma_f32_16x16x32_bf16 v[188:191], v[180:183], v[48:51], v[188:191]
	v_mfma_f32_16x16x32_bf16 v[160:163], v[180:183], v[78:81], v[160:163]
	v_mfma_f32_16x16x32_bf16 v[168:171], v[180:183], v[52:55], v[168:171]
	v_mfma_f32_16x16x32_bf16 v[188:191], v[180:183], v[56:59], v[188:191]
	v_mfma_f32_16x16x32_bf16 v[160:163], v[180:183], v[70:73], v[160:163]
	v_mfma_f32_16x16x32_bf16 v[164:167], v[192:195], v[66:69], v[164:167]
	v_mfma_f32_16x16x32_bf16 v[176:179], v[192:195], v[102:105], v[176:179]
	v_mfma_f32_16x16x32_bf16 v[156:159], v[192:195], v[82:85], v[156:159]
	s_waitcnt lgkmcnt(1)
	v_mfma_f32_16x16x32_bf16 v[168:171], v[196:199], v[60:63], v[168:171]
	v_mfma_f32_16x16x32_bf16 v[188:191], v[196:199], v[48:51], v[188:191]
	v_mfma_f32_16x16x32_bf16 v[160:163], v[196:199], v[78:81], v[160:163]
	ds_read_b128 v[180:183], v241
	ds_read_b128 v[196:199], v242
	v_mfma_f32_16x16x32_bf16 v[164:167], v[192:195], v[74:77], v[164:167]
	v_mfma_f32_16x16x32_bf16 v[176:179], v[192:195], v[86:89], v[176:179]
	v_mfma_f32_16x16x32_bf16 v[156:159], v[192:195], v[90:93], v[156:159]
	s_waitcnt lgkmcnt(1)
	v_mfma_f32_16x16x32_bf16 v[164:167], v[180:183], v[66:69], v[164:167]
	v_mfma_f32_16x16x32_bf16 v[176:179], v[180:183], v[102:105], v[176:179]
	v_mfma_f32_16x16x32_bf16 v[156:159], v[180:183], v[82:85], v[156:159]
	v_mfma_f32_16x16x32_bf16 v[168:171], v[184:187], v[66:69], v[168:171]
	v_mfma_f32_16x16x32_bf16 v[180:183], v[184:187], v[102:105], v[188:191]
	v_mfma_f32_16x16x32_bf16 v[160:163], v[184:187], v[82:85], v[160:163]
	v_mfma_f32_16x16x32_bf16 v[168:171], v[184:187], v[74:77], v[168:171]
	v_mfma_f32_16x16x32_bf16 v[180:183], v[184:187], v[86:89], v[180:183]
	v_mfma_f32_16x16x32_bf16 v[160:163], v[184:187], v[90:93], v[160:163]
	ds_read_b128 v[184:187], v243
	ds_read_b128 v[188:191], v244
	s_waitcnt lgkmcnt(0)
	s_barrier
	v_mfma_f32_16x16x32_bf16 v[168:171], v[196:199], v[66:69], v[168:171]
	v_mfma_f32_16x16x32_bf16 v[180:183], v[196:199], v[102:105], v[180:183]
	v_mfma_f32_16x16x32_bf16 v[164:167], v[172:175], v[98:101], v[164:167]
	v_mfma_f32_16x16x32_bf16 v[176:179], v[172:175], v[106:109], v[176:179]
	v_mfma_f32_16x16x32_bf16 v[156:159], v[172:175], v[122:125], v[156:159]
	v_mfma_f32_16x16x32_bf16 v[160:163], v[196:199], v[82:85], v[160:163]
	v_mfma_f32_16x16x32_bf16 v[164:167], v[172:175], v[110:113], v[164:167]
	v_mfma_f32_16x16x32_bf16 v[176:179], v[172:175], v[114:117], v[176:179]
	v_mfma_f32_16x16x32_bf16 v[156:159], v[172:175], v[126:129], v[156:159]
	v_mfma_f32_16x16x32_bf16 v[168:171], v[200:203], v[98:101], v[168:171]
	v_mfma_f32_16x16x32_bf16 v[172:175], v[200:203], v[106:109], v[180:183]
	v_mfma_f32_16x16x32_bf16 v[160:163], v[200:203], v[122:125], v[160:163]
	v_mfma_f32_16x16x32_bf16 v[168:171], v[200:203], v[110:113], v[168:171]
	v_mfma_f32_16x16x32_bf16 v[172:175], v[200:203], v[114:117], v[172:175]
	v_mfma_f32_16x16x32_bf16 v[160:163], v[200:203], v[126:129], v[160:163]
	v_mfma_f32_16x16x32_bf16 v[164:167], v[184:187], v[98:101], v[164:167]
	v_mfma_f32_16x16x32_bf16 v[176:179], v[184:187], v[106:109], v[176:179]
	v_mfma_f32_16x16x32_bf16 v[168:171], v[188:191], v[98:101], v[168:171]
	v_mfma_f32_16x16x32_bf16 v[172:175], v[188:191], v[106:109], v[172:175]
	v_mfma_f32_16x16x32_bf16 v[156:159], v[184:187], v[122:125], v[156:159]
	s_nop 4
	ds_write2_b32 v238, v164, v176 offset1:16
	ds_write2_b32 v238, v166, v178 offset0:96 offset1:112
	s_nop 0
	ds_write2_b32 v238, v156, v165 offset0:32 offset1:48
	ds_write2_b32 v238, v177, v157 offset0:64 offset1:80
	ds_write2_b32 v238, v158, v167 offset0:128 offset1:144
	ds_write2_b32 v238, v179, v159 offset0:160 offset1:176
	v_mfma_f32_16x16x32_bf16 v[160:163], v[188:191], v[122:125], v[160:163]
	ds_write2_b32 v64, v168, v172 offset1:16
	ds_write2_b32 v64, v170, v174 offset0:96 offset1:112
	s_nop 5
	ds_write2_b32 v64, v160, v169 offset0:32 offset1:48
	ds_write2_b32 v64, v173, v161 offset0:64 offset1:80
	ds_write2_b32 v64, v162, v171 offset0:128 offset1:144
	ds_write2_b32 v64, v175, v163 offset0:160 offset1:176
	s_waitcnt lgkmcnt(0)
	s_barrier
	ds_read2st64_b32 v[156:157], v234 offset1:8
	ds_read2st64_b32 v[158:159], v234 offset0:16 offset1:24
	ds_read2st64_b32 v[160:161], v234 offset0:48 offset1:56
	ds_read2st64_b32 v[162:163], v234 offset0:64 offset1:72
	ds_read2st64_b32 v[164:165], v234 offset0:96 offset1:104
	ds_read2st64_b32 v[166:167], v234 offset0:112 offset1:120
	ds_read2st64_b32 v[168:169], v234 offset0:144 offset1:152
	s_waitcnt lgkmcnt(6)
	v_add_f32_e32 v64, 0, v156
	s_waitcnt lgkmcnt(5)
	v_add_f32_e32 v64, v64, v159
	s_waitcnt lgkmcnt(4)
	v_add_f32_e32 v64, v64, v160
	ds_read2st64_b32 v[170:171], v234 offset0:160 offset1:168
	s_waitcnt lgkmcnt(4)
	v_add_f32_e32 v64, v64, v163
	s_waitcnt lgkmcnt(3)
	v_add_f32_e32 v64, v64, v164
	s_waitcnt lgkmcnt(2)
	v_add_f32_e32 v64, v64, v167
	s_waitcnt lgkmcnt(1)
	v_add_f32_e32 v64, v64, v168
	ds_read2st64_b32 v[172:173], v234 offset0:32 offset1:40
	s_waitcnt lgkmcnt(1)
	v_add_f32_e32 v64, v64, v171
	ds_write_b32 v235, v64
	v_add_f32_e32 v64, 0, v157
	ds_read2st64_b32 v[156:157], v234 offset0:80 offset1:88
	ds_read2st64_b32 v[174:175], v234 offset0:128 offset1:136
	s_waitcnt lgkmcnt(3)
	v_add_f32_e32 v64, v64, v172
	v_add_f32_e32 v64, v64, v161
	ds_read2st64_b32 v[160:161], v234 offset0:176 offset1:184
	s_waitcnt lgkmcnt(2)
	v_add_f32_e32 v64, v64, v156
	v_add_f32_e32 v64, v64, v165
	s_waitcnt lgkmcnt(1)
	v_add_f32_e32 v64, v64, v174
	v_add_f32_e32 v64, v64, v169
	s_waitcnt lgkmcnt(0)
	v_add_f32_e32 v64, v64, v160
	v_add_u32_e32 v156, 0x800, v235
	ds_write_b32 v156, v64
	v_add_f32_e32 v64, 0, v158
	v_add_f32_e32 v64, v64, v173
	v_add_f32_e32 v64, v64, v162
	v_add_f32_e32 v64, v64, v157
	v_add_f32_e32 v64, v64, v166
	v_add_f32_e32 v64, v64, v175
	v_add_f32_e32 v64, v64, v170
	v_add_f32_e32 v64, v64, v161
	v_add_u32_e32 v156, 0x1000, v235
	ds_write_b32 v156, v64
	s_waitcnt lgkmcnt(0)
	s_barrier
	s_and_saveexec_b64 s[22:23], s[6:7]
	s_cbranch_execz .LBB0_696
	v_mov_b32_e32 v160, 0x24000
	ds_read_b128 v[160:163], v160
	ds_read_b128 v[156:159], v231
	v_mov_b32_e32 v176, 0x7f800000
	s_waitcnt lgkmcnt(0)
	v_pk_add_f32 v[156:157], v[156:157], v[160:161]
	s_nop 0
	v_cmp_gt_f32_e64 s[10:11], v157, v156
	v_add_f32_e32 v64, v158, v162
	v_add_f32_e32 v158, v159, v163
	v_cndmask_b32_e64 v159, v156, v157, s[10:11]
	v_cmp_gt_f32_e32 vcc, v64, v159
	s_nop 1
	v_cndmask_b32_e32 v159, v159, v64, vcc
	v_cmp_gt_f32_e64 s[8:9], v158, v159
	s_nop 1
	v_cndmask_b32_e64 v159, v159, v158, s[8:9]
	v_sub_f32_e32 v172, v156, v159
	v_sub_f32_e32 v156, v157, v159
	v_mul_f32_e32 v157, 0x3fb8aa3b, v156
	v_fma_f32 v160, v156, s33, -v157
	v_rndne_f32_e32 v161, v157
	v_fmac_f32_e32 v160, 0x32a5705f, v156
	v_sub_f32_e32 v157, v157, v161
	v_add_f32_e32 v157, v157, v160
	v_exp_f32_e32 v157, v157
	v_cvt_i32_f32_e32 v160, v161
	v_cmp_ngt_f32_e64 s[12:13], s54, v156
	v_sub_f32_e32 v64, v64, v159
	v_ldexp_f32 v157, v157, v160
	v_cndmask_b32_e64 v157, 0, v157, s[12:13]
	v_cmp_nlt_f32_e64 s[12:13], s85, v156
	v_mul_f32_e32 v156, 0x3fb8aa3b, v64
	v_rndne_f32_e32 v160, v156
	v_cndmask_b32_e64 v173, v176, v157, s[12:13]
	v_fma_f32 v157, v64, s33, -v156
	v_fmac_f32_e32 v157, 0x32a5705f, v64
	v_sub_f32_e32 v156, v156, v160
	v_add_f32_e32 v156, v156, v157
	v_exp_f32_e32 v156, v156
	v_cvt_i32_f32_e32 v157, v160
	v_cmp_ngt_f32_e64 s[12:13], s54, v64
	v_ldexp_f32 v156, v156, v157
	s_nop 0
	v_cndmask_b32_e64 v156, 0, v156, s[12:13]
	v_cmp_nlt_f32_e64 s[12:13], s85, v64
	s_nop 1
	v_cndmask_b32_e64 v64, v176, v156, s[12:13]
	v_sub_f32_e32 v156, v158, v159
	v_mul_f32_e32 v157, 0x3fb8aa3b, v156
	v_fma_f32 v158, v156, s33, -v157
	v_rndne_f32_e32 v159, v157
	v_fmac_f32_e32 v158, 0x32a5705f, v156
	v_sub_f32_e32 v157, v157, v159
	v_add_f32_e32 v157, v157, v158
	v_exp_f32_e32 v157, v157
	v_cvt_i32_f32_e32 v158, v159
	v_cmp_ngt_f32_e64 s[12:13], s54, v156
	v_ldexp_f32 v157, v157, v158
	s_nop 0
	v_cndmask_b32_e64 v157, 0, v157, s[12:13]
	v_cmp_nlt_f32_e64 s[12:13], s85, v156
	v_cndmask_b32_e64 v156, 0, 8, s[10:11]
	v_cndmask_b32_e64 v156, v156, 16, vcc
	v_cndmask_b32_e64 v175, v156, 24, s[8:9]
	v_lshlrev_b32_e32 v168, 2, v175
	v_add_u32_e32 v160, v231, v168
	v_cndmask_b32_e64 v174, v176, v157, s[12:13]
	ds_read_b128 v[156:159], v160 offset:16
	ds_read_b128 v[160:163], v160 offset:32
	v_add_u32_e32 v164, 0x24000, v168
	ds_read_b128 v[168:171], v164 offset:16
	ds_read_b128 v[164:167], v164 offset:32
	v_cmp_ngt_f32_e32 vcc, s54, v172
	s_mov_b32 s12, 0xff61b1e6
	s_waitcnt lgkmcnt(0)
	v_add_f32_e32 v160, v160, v164
	v_mul_f32_e32 v164, 0x3fb8aa3b, v172
	v_add_f32_e32 v161, v161, v165
	v_add_f32_e32 v162, v162, v166
	v_fma_f32 v165, v172, s33, -v164
	v_rndne_f32_e32 v166, v164
	v_fmac_f32_e32 v165, 0x32a5705f, v172
	v_sub_f32_e32 v164, v164, v166
	v_add_f32_e32 v164, v164, v165
	v_exp_f32_e32 v164, v164
	v_cvt_i32_f32_e32 v165, v166
	v_pk_add_f32 v[156:157], v[156:157], v[168:169]
	v_add_f32_e32 v158, v158, v170
	v_add_f32_e32 v159, v159, v171
	v_ldexp_f32 v164, v164, v165
	v_cndmask_b32_e32 v164, 0, v164, vcc
	v_cmp_nlt_f32_e32 vcc, s85, v172
	v_add_f32_e32 v163, v163, v167
	v_cmp_nlt_f32_e64 s[12:13], s12, v156
	v_cndmask_b32_e32 v164, v176, v164, vcc
	v_cmp_gt_f32_e32 vcc, v157, v156
	v_add_f32_e32 v164, v164, v173
	v_add_f32_e32 v64, v64, v164
	v_cndmask_b32_e32 v165, v156, v157, vcc
	v_cndmask_b32_e64 v164, 0, 1, vcc
	v_cmp_gt_f32_e32 vcc, v158, v165
	v_mov_b32_e32 v166, 0xff61b1e6
	v_add_f32_e32 v64, v174, v64
	v_cndmask_b32_e32 v165, v165, v158, vcc
	v_cndmask_b32_e64 v164, v164, 2, vcc
	v_cmp_gt_f32_e32 vcc, v159, v165
	s_nop 1
	v_cndmask_b32_e32 v165, v165, v159, vcc
	v_cndmask_b32_e64 v164, v164, 3, vcc
	v_cmp_gt_f32_e32 vcc, v160, v165
	s_nop 1
	v_cndmask_b32_e32 v165, v165, v160, vcc
	v_cndmask_b32_e64 v164, v164, 4, vcc
	v_cmp_gt_f32_e32 vcc, v161, v165
	s_nop 1
	v_cndmask_b32_e32 v165, v165, v161, vcc
	v_cndmask_b32_e64 v164, v164, 5, vcc
	v_cmp_gt_f32_e32 vcc, v162, v165
	s_nop 1
	v_cndmask_b32_e32 v165, v165, v162, vcc
	v_cndmask_b32_e64 v164, v164, 6, vcc
	v_cmp_ngt_f32_e64 s[8:9], v163, v165
	s_nop 1
	v_cndmask_b32_e64 v164, 7, v164, s[8:9]
	v_cmp_eq_u32_e64 s[10:11], 0, v164
	s_or_b64 s[12:13], s[10:11], s[12:13]
	v_cndmask_b32_e64 v156, v156, v166, s[12:13]
	v_cmp_ne_u32_e64 s[12:13], 1, v164
	v_cmp_gt_f32_e64 s[14:15], v157, v156
	s_and_b64 s[12:13], s[12:13], s[14:15]
	s_or_b64 s[10:11], s[10:11], s[12:13]
	v_cndmask_b32_e64 v156, v156, v157, s[12:13]
	v_cndmask_b32_e64 v157, 0, 1, s[10:11]
	v_cmp_ne_u32_e64 s[10:11], 2, v164
	v_cmp_gt_f32_e64 s[12:13], v158, v156
	s_and_b64 s[10:11], s[10:11], s[12:13]
	v_cndmask_b32_e64 v156, v156, v158, s[10:11]
	v_cndmask_b32_e64 v157, v157, 2, s[10:11]
	v_cmp_ne_u32_e64 s[10:11], 3, v164
	v_cmp_gt_f32_e64 s[12:13], v159, v156
	s_and_b64 s[10:11], s[10:11], s[12:13]
	v_cndmask_b32_e64 v156, v156, v159, s[10:11]
	v_cndmask_b32_e64 v157, v157, 3, s[10:11]
	v_cmp_ne_u32_e64 s[10:11], 4, v164
	v_cmp_gt_f32_e64 s[12:13], v160, v156
	s_and_b64 s[10:11], s[10:11], s[12:13]
	v_cndmask_b32_e64 v156, v156, v160, s[10:11]
	v_cndmask_b32_e64 v157, v157, 4, s[10:11]
	v_cmp_ne_u32_e64 s[10:11], 5, v164
	v_cmp_gt_f32_e64 s[12:13], v161, v156
	s_and_b64 s[10:11], s[10:11], s[12:13]
	v_cndmask_b32_e64 v156, v156, v161, s[10:11]
	v_cndmask_b32_e64 v157, v157, 5, s[10:11]
	s_and_b64 s[10:11], vcc, s[8:9]
	v_cmp_ngt_f32_e32 vcc, v162, v156
	s_or_b64 vcc, s[10:11], vcc
	v_cndmask_b32_e64 v165, v163, v165, s[8:9]
	v_cndmask_b32_e32 v156, v162, v156, vcc
	v_cndmask_b32_e32 v157, 6, v157, vcc
	v_cmp_gt_f32_e32 vcc, v163, v156
	s_and_b64 vcc, s[8:9], vcc
	s_nop 0
	v_cndmask_b32_e64 v159, v157, 7, vcc
	v_div_scale_f32 v157, s[8:9], v64, v64, 1.0
	v_rcp_f32_e32 v158, v157
	v_cndmask_b32_e32 v156, v156, v163, vcc
	v_sub_f32_e32 v156, v156, v165
	v_add_u32_e32 v159, v159, v175
	v_fma_f32 v160, -v157, v158, 1.0
	v_fmac_f32_e32 v158, v160, v158
	v_div_scale_f32 v160, vcc, 1.0, v64, 1.0
	v_mul_f32_e32 v161, v160, v158
	v_fma_f32 v162, -v157, v161, v160
	v_fmac_f32_e32 v161, v162, v158
	v_fma_f32 v157, -v157, v161, v160
	v_div_fmas_f32 v157, v157, v158, v161
	v_div_fixup_f32 v64, v157, v64, 1.0
	v_mul_f32_e32 v157, 0x3fb8aa3b, v156
	v_fma_f32 v158, v156, s33, -v157
	v_rndne_f32_e32 v160, v157
	v_fmac_f32_e32 v158, 0x32a5705f, v156
	v_sub_f32_e32 v157, v157, v160
	v_add_f32_e32 v157, v157, v158
	v_exp_f32_e32 v157, v157
	v_cvt_i32_f32_e32 v158, v160
	v_cmp_ngt_f32_e32 vcc, s54, v156
	v_ldexp_f32 v157, v157, v158
	s_nop 0
	v_cndmask_b32_e32 v157, 0, v157, vcc
	v_cmp_nlt_f32_e32 vcc, s85, v156
	s_nop 1
	v_cndmask_b32_e32 v157, v176, v157, vcc
	v_add_f32_e32 v156, 1.0, v157
	v_div_scale_f32 v158, s[8:9], v156, v156, 1.0
	v_rcp_f32_e32 v160, v158
	s_add_i32 s8, 0, 0x22c00
	v_fma_f32 v161, -v158, v160, 1.0
	v_fmac_f32_e32 v160, v161, v160
	v_div_scale_f32 v161, vcc, 1.0, v156, 1.0
	v_mul_f32_e32 v162, v161, v160
	v_fma_f32 v163, -v158, v162, v161
	v_fmac_f32_e32 v162, v163, v160
	v_fma_f32 v158, -v158, v162, v161
	v_div_fmas_f32 v158, v158, v160, v162
	v_div_fixup_f32 v156, v158, v156, 1.0
	v_or_b32_e32 v158, v164, v175
	ds_write_b64 v237, v[158:159]
	v_lshl_add_u32 v158, v158, 2, s8
	v_mov_b32_e32 v160, 1
	ds_add_rtn_u32 v158, v158, v160
	v_mul_f32_e32 v157, v157, v156
	v_pk_mul_f32 v[156:157], v[64:65], v[156:157] op_sel_hi:[0,1]
	s_waitcnt lgkmcnt(0)
	ds_write_b32 v237, v158 offset:2048
	v_lshl_add_u32 v158, v159, 2, s8
	ds_add_rtn_u32 v158, v158, v160
	s_waitcnt lgkmcnt(0)
	ds_write_b32 v237, v158 offset:2052
	v_lshl_add_u64 v[158:159], s[42:43], 0, v[148:149]
	global_store_dwordx2 v[158:159], v[156:157], off
	s_branch .LBB0_696
